# hand-written HGRN chunk chain: 4 state elements per thread (x4 loads, x2 stores), 16 chunks in flight, waves 0-1 of every WG
# baseline (speedup 1.0000x reference)
; #define H2_LOAD(V, D, C0) do { _Pragma("unroll") for (int u = 0; u < 6; ++u) { V[u] = __builtin_nontemporal_load(kv + (size_t)((C0) + u) * 8 * 16384); D[u] = dc[(size_t)((C0) + u) * 8 * 128]; } } while (0)
; #define H2_STEP(V, D, C0) do { _Pragma("unroll") for (int u = 0; u < 6; ++u) { sb[(size_t)((C0) + u) * 8 * 16384] = f2bf(S); S = fmaf(D[u], S, V[u]); } } while (0)
; __device__ __forceinline__ void ph_hgrn_chain2(const P& p, int gt, int nt) {
;   for (int idx = gt; idx < 8 * 128 * 128; idx += nt) {
;     const int hd = idx >> 14, ed = idx & 16383, d = ed & 127;
;     const float* kv = WSP(float, WS_KVC) + (size_t)hd * 16384 + ed; const float* dc = WSP(float, WS_DEC) + hd * 128 + d; bf16_t* sb = WSP(bf16_t, WS_SB) + (size_t)hd * 16384 + ed;
;     float S = 0.f;
;     float a[6], da[6], b2[6], db[6];
;     ...
;     H2_LOAD(a, da, 0);
; #pragma unroll 1
;     for (int c0 = 0; c0 < HG_NCH; c0 += 12) {
;       H2_LOAD(b2, db, c0 + 6); H2_STEP(a, da, c0);
;       if (c0 + 12 < HG_NCH) H2_LOAD(a, da, c0 + 12);
;       H2_STEP(b2, db, c0 + 6);
;     }
; __global__ void __launch_bounds__(NTHR, 2) mega(MArgs a) {
;     ...
;     if (IN(b + 3)) { LDP();
;       if (l == 0 && G > 16) { if ((int)blockIdx.x >= 8) ph_hgrn_chain2(p, gt - 8 * NTHR, nt - 8 * NTHR); }
;       else ph_hgrn_chain2(p, gt, nt);
.LBB0_393:
	s_andn2_b64 vcc, exec, s[0:1]
	s_cbranch_vccnz .LBB0_526
	v_readlane_b32 s0, v252, 0
	v_readlane_b32 s1, v252, 1
	v_mov_b32_e32 v0, v97
	s_load_dwordx2 s[12:13], s[0:1], 0x60
	s_nop 0
	s_load_dwordx2 s[0:1], s[0:1], 0xe0
	v_readlane_b32 s3, v252, 5
	v_mbcnt_lo_u32_b32 v0, -1, v0
	v_mbcnt_hi_u32_b32 v12, -1, v0
	v_readlane_b32 s2, v252, 6
	s_mov_b32 s4, s81
	v_readlane_b32 s6, v255, 18
	v_readlane_b32 s4, v253, 31
	v_readlane_b32 s3, v252, 11
	v_readlane_b32 s5, v253, 32
	v_readlane_b32 s7, v255, 19
	v_add_u32_e32 v196, s3, v12
	v_readlane_b32 s3, v254, 61
	s_and_b64 s[4:5], s[4:5], s[6:7]
	s_andn2_b64 vcc, exec, s[4:5]
	v_add_u32_e32 v13, s3, v196
	s_mov_b64 s[6:7], -1
	v_readlane_b32 s3, v252, 4
	s_nop 3
	s_cmp_gt_u32 s3, 1
	s_cbranch_scc1 .Lchain_done
	s_waitcnt lgkmcnt(0)
	s_lshl_b32 s4, s3, 6
	s_lshl_b32 s5, s88, 7
	s_add_i32 s4, s4, s5
	v_add_u32_e32 v0, s4, v12
	v_lshrrev_b32_e32 v1, 12, v0
	v_and_b32_e32 v2, 0xfff, v0
	v_lshlrev_b32_e32 v3, 16, v1
	v_lshl_add_u32 v3, v2, 4, v3
	v_lshlrev_b32_e32 v4, 15, v1
	v_lshl_add_u32 v4, v2, 3, v4
	v_and_b32_e32 v5, 31, v0
	v_lshlrev_b32_e32 v6, 9, v1
	v_lshl_add_u32 v5, v5, 4, v6
	s_add_u32 s14, s0, 0x33b5e000
	s_addc_u32 s15, s1, 0
	s_add_u32 s18, s0, 0x37d5e000
	s_addc_u32 s19, s1, 0
	s_add_u32 s20, s0, 0x31a14000
	s_addc_u32 s21, s1, 0
	v_mov_b32_e32 v24, 0
	v_mov_b32_e32 v25, 0
	v_mov_b32_e32 v26, 0
	v_mov_b32_e32 v27, 0
	global_load_dwordx4 v[32:35], v3, s[14:15] nt
	global_load_dwordx4 v[36:39], v5, s[18:19]
	s_add_u32 s14, s14, 0x80000
	s_addc_u32 s15, s15, 0
	s_add_u32 s18, s18, 0x1000
	s_addc_u32 s19, s19, 0
	global_load_dwordx4 v[40:43], v3, s[14:15] nt
	global_load_dwordx4 v[44:47], v5, s[18:19]
	s_add_u32 s14, s14, 0x80000
	s_addc_u32 s15, s15, 0
	s_add_u32 s18, s18, 0x1000
	s_addc_u32 s19, s19, 0
	global_load_dwordx4 v[48:51], v3, s[14:15] nt
	global_load_dwordx4 v[52:55], v5, s[18:19]
	s_add_u32 s14, s14, 0x80000
	s_addc_u32 s15, s15, 0
	s_add_u32 s18, s18, 0x1000
	s_addc_u32 s19, s19, 0
	global_load_dwordx4 v[56:59], v3, s[14:15] nt
	global_load_dwordx4 v[60:63], v5, s[18:19]
	s_add_u32 s14, s14, 0x80000
	s_addc_u32 s15, s15, 0
	s_add_u32 s18, s18, 0x1000
	s_addc_u32 s19, s19, 0
	global_load_dwordx4 v[72:75], v3, s[14:15] nt
	global_load_dwordx4 v[76:79], v5, s[18:19]
	s_add_u32 s14, s14, 0x80000
	s_addc_u32 s15, s15, 0
	s_add_u32 s18, s18, 0x1000
	s_addc_u32 s19, s19, 0
	global_load_dwordx4 v[80:83], v3, s[14:15] nt
	global_load_dwordx4 v[84:87], v5, s[18:19]
	s_add_u32 s14, s14, 0x80000
	s_addc_u32 s15, s15, 0
	s_add_u32 s18, s18, 0x1000
	s_addc_u32 s19, s19, 0
	global_load_dwordx4 v[88:91], v3, s[14:15] nt
	global_load_dwordx4 v[92:95], v5, s[18:19]
	s_add_u32 s14, s14, 0x80000
	s_addc_u32 s15, s15, 0
	s_add_u32 s18, s18, 0x1000
	s_addc_u32 s19, s19, 0
	global_load_dwordx4 v[100:103], v3, s[14:15] nt
	global_load_dwordx4 v[104:107], v5, s[18:19]
	s_add_u32 s14, s14, 0x80000
	s_addc_u32 s15, s15, 0
	s_add_u32 s18, s18, 0x1000
	s_addc_u32 s19, s19, 0
	global_load_dwordx4 v[108:111], v3, s[14:15] nt
	global_load_dwordx4 v[112:115], v5, s[18:19]
	s_add_u32 s14, s14, 0x80000
	s_addc_u32 s15, s15, 0
	s_add_u32 s18, s18, 0x1000
	s_addc_u32 s19, s19, 0
	global_load_dwordx4 v[116:119], v3, s[14:15] nt
	global_load_dwordx4 v[120:123], v5, s[18:19]
	s_add_u32 s14, s14, 0x80000
	s_addc_u32 s15, s15, 0
	s_add_u32 s18, s18, 0x1000
	s_addc_u32 s19, s19, 0
	global_load_dwordx4 v[124:127], v3, s[14:15] nt
	global_load_dwordx4 v[128:131], v5, s[18:19]
	s_add_u32 s14, s14, 0x80000
	s_addc_u32 s15, s15, 0
	s_add_u32 s18, s18, 0x1000
	s_addc_u32 s19, s19, 0
	global_load_dwordx4 v[132:135], v3, s[14:15] nt
	global_load_dwordx4 v[136:139], v5, s[18:19]
	s_add_u32 s14, s14, 0x80000
	s_addc_u32 s15, s15, 0
	s_add_u32 s18, s18, 0x1000
	s_addc_u32 s19, s19, 0
	global_load_dwordx4 v[140:143], v3, s[14:15] nt
	global_load_dwordx4 v[144:147], v5, s[18:19]
	s_add_u32 s14, s14, 0x80000
	s_addc_u32 s15, s15, 0
	s_add_u32 s18, s18, 0x1000
	s_addc_u32 s19, s19, 0
	global_load_dwordx4 v[148:151], v3, s[14:15] nt
	global_load_dwordx4 v[152:155], v5, s[18:19]
	s_add_u32 s14, s14, 0x80000
	s_addc_u32 s15, s15, 0
	s_add_u32 s18, s18, 0x1000
	s_addc_u32 s19, s19, 0
	global_load_dwordx4 v[156:159], v3, s[14:15] nt
	global_load_dwordx4 v[160:163], v5, s[18:19]
	s_add_u32 s14, s14, 0x80000
	s_addc_u32 s15, s15, 0
	s_add_u32 s18, s18, 0x1000
	s_addc_u32 s19, s19, 0
	global_load_dwordx4 v[164:167], v3, s[14:15] nt
	global_load_dwordx4 v[168:171], v5, s[18:19]
	s_add_u32 s14, s14, 0x80000
	s_addc_u32 s15, s15, 0
	s_add_u32 s18, s18, 0x1000
	s_addc_u32 s19, s19, 0
	s_waitcnt vmcnt(30)
	v_cvt_pk_bf16_f32 v28, v24, v25
	v_cvt_pk_bf16_f32 v29, v26, v27
	v_fma_f32 v24, v36, v24, v32
	v_fma_f32 v25, v37, v25, v33
	v_fma_f32 v26, v38, v26, v34
	v_fma_f32 v27, v39, v27, v35
	global_store_dwordx2 v4, v[28:29], s[20:21]
	s_add_u32 s20, s20, 0x40000
	s_addc_u32 s21, s21, 0
	global_load_dwordx4 v[32:35], v3, s[14:15] nt
	global_load_dwordx4 v[36:39], v5, s[18:19]
	s_add_u32 s14, s14, 0x80000
	s_addc_u32 s15, s15, 0
	s_add_u32 s18, s18, 0x1000
	s_addc_u32 s19, s19, 0
	s_waitcnt vmcnt(31)
	v_cvt_pk_bf16_f32 v28, v24, v25
	v_cvt_pk_bf16_f32 v29, v26, v27
	v_fma_f32 v24, v44, v24, v40
	v_fma_f32 v25, v45, v25, v41
	v_fma_f32 v26, v46, v26, v42
	v_fma_f32 v27, v47, v27, v43
	global_store_dwordx2 v4, v[28:29], s[20:21]
	s_add_u32 s20, s20, 0x40000
	s_addc_u32 s21, s21, 0
	global_load_dwordx4 v[40:43], v3, s[14:15] nt
	global_load_dwordx4 v[44:47], v5, s[18:19]
	s_add_u32 s14, s14, 0x80000
	s_addc_u32 s15, s15, 0
	s_add_u32 s18, s18, 0x1000
	s_addc_u32 s19, s19, 0
	s_waitcnt vmcnt(32)
; #define H2_LOAD(V, D, C0) do { _Pragma("unroll") for (int u = 0; u < 6; ++u) { V[u] = __builtin_nontemporal_load(kv + (size_t)((C0) + u) * 8 * 16384); D[u] = dc[(size_t)((C0) + u) * 8 * 128]; } } while (0)
; #define H2_STEP(V, D, C0) do { _Pragma("unroll") for (int u = 0; u < 6; ++u) { sb[(size_t)((C0) + u) * 8 * 16384] = f2bf(S); S = fmaf(D[u], S, V[u]); } } while (0)
; __device__ __forceinline__ void ph_hgrn_chain2(const P& p, int gt, int nt) {
;     ...
;     H2_LOAD(a, da, 0);
; #pragma unroll 1
;     for (int c0 = 0; c0 < HG_NCH; c0 += 12) {
;       H2_LOAD(b2, db, c0 + 6); H2_STEP(a, da, c0);
;       if (c0 + 12 < HG_NCH) H2_LOAD(a, da, c0 + 12);
;       H2_STEP(b2, db, c0 + 6);
	v_cvt_pk_bf16_f32 v28, v24, v25
	v_cvt_pk_bf16_f32 v29, v26, v27
	v_fma_f32 v24, v52, v24, v48
	v_fma_f32 v25, v53, v25, v49
	v_fma_f32 v26, v54, v26, v50
	v_fma_f32 v27, v55, v27, v51
	global_store_dwordx2 v4, v[28:29], s[20:21]
	s_add_u32 s20, s20, 0x40000
	s_addc_u32 s21, s21, 0
	global_load_dwordx4 v[48:51], v3, s[14:15] nt
	global_load_dwordx4 v[52:55], v5, s[18:19]
	s_add_u32 s14, s14, 0x80000
	s_addc_u32 s15, s15, 0
	s_add_u32 s18, s18, 0x1000
	s_addc_u32 s19, s19, 0
	s_waitcnt vmcnt(33)
	v_cvt_pk_bf16_f32 v28, v24, v25
	v_cvt_pk_bf16_f32 v29, v26, v27
	v_fma_f32 v24, v60, v24, v56
	v_fma_f32 v25, v61, v25, v57
	v_fma_f32 v26, v62, v26, v58
	v_fma_f32 v27, v63, v27, v59
	global_store_dwordx2 v4, v[28:29], s[20:21]
	s_add_u32 s20, s20, 0x40000
	s_addc_u32 s21, s21, 0
	global_load_dwordx4 v[56:59], v3, s[14:15] nt
	global_load_dwordx4 v[60:63], v5, s[18:19]
	s_add_u32 s14, s14, 0x80000
	s_addc_u32 s15, s15, 0
	s_add_u32 s18, s18, 0x1000
	s_addc_u32 s19, s19, 0
	s_waitcnt vmcnt(34)
	v_cvt_pk_bf16_f32 v28, v24, v25
	v_cvt_pk_bf16_f32 v29, v26, v27
	v_fma_f32 v24, v76, v24, v72
	v_fma_f32 v25, v77, v25, v73
	v_fma_f32 v26, v78, v26, v74
	v_fma_f32 v27, v79, v27, v75
	global_store_dwordx2 v4, v[28:29], s[20:21]
	s_add_u32 s20, s20, 0x40000
	s_addc_u32 s21, s21, 0
	global_load_dwordx4 v[72:75], v3, s[14:15] nt
	global_load_dwordx4 v[76:79], v5, s[18:19]
	s_add_u32 s14, s14, 0x80000
	s_addc_u32 s15, s15, 0
	s_add_u32 s18, s18, 0x1000
	s_addc_u32 s19, s19, 0
	s_waitcnt vmcnt(35)
	v_cvt_pk_bf16_f32 v28, v24, v25
	v_cvt_pk_bf16_f32 v29, v26, v27
	v_fma_f32 v24, v84, v24, v80
	v_fma_f32 v25, v85, v25, v81
	v_fma_f32 v26, v86, v26, v82
	v_fma_f32 v27, v87, v27, v83
	global_store_dwordx2 v4, v[28:29], s[20:21]
	s_add_u32 s20, s20, 0x40000
	s_addc_u32 s21, s21, 0
	global_load_dwordx4 v[80:83], v3, s[14:15] nt
	global_load_dwordx4 v[84:87], v5, s[18:19]
	s_add_u32 s14, s14, 0x80000
	s_addc_u32 s15, s15, 0
	s_add_u32 s18, s18, 0x1000
	s_addc_u32 s19, s19, 0
	s_waitcnt vmcnt(36)
	v_cvt_pk_bf16_f32 v28, v24, v25
	v_cvt_pk_bf16_f32 v29, v26, v27
	v_fma_f32 v24, v92, v24, v88
	v_fma_f32 v25, v93, v25, v89
	v_fma_f32 v26, v94, v26, v90
	v_fma_f32 v27, v95, v27, v91
	global_store_dwordx2 v4, v[28:29], s[20:21]
	s_add_u32 s20, s20, 0x40000
	s_addc_u32 s21, s21, 0
	global_load_dwordx4 v[88:91], v3, s[14:15] nt
	global_load_dwordx4 v[92:95], v5, s[18:19]
	s_add_u32 s14, s14, 0x80000
	s_addc_u32 s15, s15, 0
	s_add_u32 s18, s18, 0x1000
	s_addc_u32 s19, s19, 0
	s_waitcnt vmcnt(37)
	v_cvt_pk_bf16_f32 v28, v24, v25
	v_cvt_pk_bf16_f32 v29, v26, v27
	v_fma_f32 v24, v104, v24, v100
	v_fma_f32 v25, v105, v25, v101
	v_fma_f32 v26, v106, v26, v102
	v_fma_f32 v27, v107, v27, v103
	global_store_dwordx2 v4, v[28:29], s[20:21]
	s_add_u32 s20, s20, 0x40000
	s_addc_u32 s21, s21, 0
	global_load_dwordx4 v[100:103], v3, s[14:15] nt
	global_load_dwordx4 v[104:107], v5, s[18:19]
	s_add_u32 s14, s14, 0x80000
	s_addc_u32 s15, s15, 0
	s_add_u32 s18, s18, 0x1000
	s_addc_u32 s19, s19, 0
	s_waitcnt vmcnt(38)
	v_cvt_pk_bf16_f32 v28, v24, v25
	v_cvt_pk_bf16_f32 v29, v26, v27
	v_fma_f32 v24, v112, v24, v108
	v_fma_f32 v25, v113, v25, v109
	v_fma_f32 v26, v114, v26, v110
	v_fma_f32 v27, v115, v27, v111
	global_store_dwordx2 v4, v[28:29], s[20:21]
	s_add_u32 s20, s20, 0x40000
	s_addc_u32 s21, s21, 0
	global_load_dwordx4 v[108:111], v3, s[14:15] nt
	global_load_dwordx4 v[112:115], v5, s[18:19]
	s_add_u32 s14, s14, 0x80000
	s_addc_u32 s15, s15, 0
	s_add_u32 s18, s18, 0x1000
	s_addc_u32 s19, s19, 0
	s_waitcnt vmcnt(39)
	v_cvt_pk_bf16_f32 v28, v24, v25
	v_cvt_pk_bf16_f32 v29, v26, v27
	v_fma_f32 v24, v120, v24, v116
	v_fma_f32 v25, v121, v25, v117
	v_fma_f32 v26, v122, v26, v118
	v_fma_f32 v27, v123, v27, v119
	global_store_dwordx2 v4, v[28:29], s[20:21]
	s_add_u32 s20, s20, 0x40000
	s_addc_u32 s21, s21, 0
	global_load_dwordx4 v[116:119], v3, s[14:15] nt
	global_load_dwordx4 v[120:123], v5, s[18:19]
	s_add_u32 s14, s14, 0x80000
	s_addc_u32 s15, s15, 0
	s_add_u32 s18, s18, 0x1000
	s_addc_u32 s19, s19, 0
	s_waitcnt vmcnt(40)
	v_cvt_pk_bf16_f32 v28, v24, v25
	v_cvt_pk_bf16_f32 v29, v26, v27
	v_fma_f32 v24, v128, v24, v124
	v_fma_f32 v25, v129, v25, v125
	v_fma_f32 v26, v130, v26, v126
	v_fma_f32 v27, v131, v27, v127
	global_store_dwordx2 v4, v[28:29], s[20:21]
	s_add_u32 s20, s20, 0x40000
	s_addc_u32 s21, s21, 0
	global_load_dwordx4 v[124:127], v3, s[14:15] nt
	global_load_dwordx4 v[128:131], v5, s[18:19]
	s_add_u32 s14, s14, 0x80000
	s_addc_u32 s15, s15, 0
	s_add_u32 s18, s18, 0x1000
	s_addc_u32 s19, s19, 0
	s_waitcnt vmcnt(41)
	v_cvt_pk_bf16_f32 v28, v24, v25
	v_cvt_pk_bf16_f32 v29, v26, v27
	v_fma_f32 v24, v136, v24, v132
	v_fma_f32 v25, v137, v25, v133
	v_fma_f32 v26, v138, v26, v134
	v_fma_f32 v27, v139, v27, v135
	global_store_dwordx2 v4, v[28:29], s[20:21]
	s_add_u32 s20, s20, 0x40000
	s_addc_u32 s21, s21, 0
	global_load_dwordx4 v[132:135], v3, s[14:15] nt
	global_load_dwordx4 v[136:139], v5, s[18:19]
	s_add_u32 s14, s14, 0x80000
	s_addc_u32 s15, s15, 0
	s_add_u32 s18, s18, 0x1000
	s_addc_u32 s19, s19, 0
	s_waitcnt vmcnt(42)
	v_cvt_pk_bf16_f32 v28, v24, v25
	v_cvt_pk_bf16_f32 v29, v26, v27
	v_fma_f32 v24, v144, v24, v140
	v_fma_f32 v25, v145, v25, v141
	v_fma_f32 v26, v146, v26, v142
	v_fma_f32 v27, v147, v27, v143
	global_store_dwordx2 v4, v[28:29], s[20:21]
	s_add_u32 s20, s20, 0x40000
	s_addc_u32 s21, s21, 0
	global_load_dwordx4 v[140:143], v3, s[14:15] nt
	global_load_dwordx4 v[144:147], v5, s[18:19]
	s_add_u32 s14, s14, 0x80000
	s_addc_u32 s15, s15, 0
	s_add_u32 s18, s18, 0x1000
	s_addc_u32 s19, s19, 0
	s_waitcnt vmcnt(43)
; #define H2_LOAD(V, D, C0) do { _Pragma("unroll") for (int u = 0; u < 6; ++u) { V[u] = __builtin_nontemporal_load(kv + (size_t)((C0) + u) * 8 * 16384); D[u] = dc[(size_t)((C0) + u) * 8 * 128]; } } while (0)
; #define H2_STEP(V, D, C0) do { _Pragma("unroll") for (int u = 0; u < 6; ++u) { sb[(size_t)((C0) + u) * 8 * 16384] = f2bf(S); S = fmaf(D[u], S, V[u]); } } while (0)
; __device__ __forceinline__ void ph_hgrn_chain2(const P& p, int gt, int nt) {
;     ...
;     H2_LOAD(a, da, 0);
; #pragma unroll 1
;     for (int c0 = 0; c0 < HG_NCH; c0 += 12) {
;       H2_LOAD(b2, db, c0 + 6); H2_STEP(a, da, c0);
;       if (c0 + 12 < HG_NCH) H2_LOAD(a, da, c0 + 12);
;       H2_STEP(b2, db, c0 + 6);
	v_cvt_pk_bf16_f32 v28, v24, v25
	v_cvt_pk_bf16_f32 v29, v26, v27
	v_fma_f32 v24, v152, v24, v148
	v_fma_f32 v25, v153, v25, v149
	v_fma_f32 v26, v154, v26, v150
	v_fma_f32 v27, v155, v27, v151
	global_store_dwordx2 v4, v[28:29], s[20:21]
	s_add_u32 s20, s20, 0x40000
	s_addc_u32 s21, s21, 0
	global_load_dwordx4 v[148:151], v3, s[14:15] nt
	global_load_dwordx4 v[152:155], v5, s[18:19]
	s_add_u32 s14, s14, 0x80000
	s_addc_u32 s15, s15, 0
	s_add_u32 s18, s18, 0x1000
	s_addc_u32 s19, s19, 0
	s_waitcnt vmcnt(44)
	v_cvt_pk_bf16_f32 v28, v24, v25
	v_cvt_pk_bf16_f32 v29, v26, v27
	v_fma_f32 v24, v160, v24, v156
	v_fma_f32 v25, v161, v25, v157
	v_fma_f32 v26, v162, v26, v158
	v_fma_f32 v27, v163, v27, v159
	global_store_dwordx2 v4, v[28:29], s[20:21]
	s_add_u32 s20, s20, 0x40000
	s_addc_u32 s21, s21, 0
	global_load_dwordx4 v[156:159], v3, s[14:15] nt
	global_load_dwordx4 v[160:163], v5, s[18:19]
	s_add_u32 s14, s14, 0x80000
	s_addc_u32 s15, s15, 0
	s_add_u32 s18, s18, 0x1000
	s_addc_u32 s19, s19, 0
	s_waitcnt vmcnt(45)
	v_cvt_pk_bf16_f32 v28, v24, v25
	v_cvt_pk_bf16_f32 v29, v26, v27
	v_fma_f32 v24, v168, v24, v164
	v_fma_f32 v25, v169, v25, v165
	v_fma_f32 v26, v170, v26, v166
	v_fma_f32 v27, v171, v27, v167
	global_store_dwordx2 v4, v[28:29], s[20:21]
	s_add_u32 s20, s20, 0x40000
	s_addc_u32 s21, s21, 0
	global_load_dwordx4 v[164:167], v3, s[14:15] nt
	global_load_dwordx4 v[168:171], v5, s[18:19]
	s_add_u32 s14, s14, 0x80000
	s_addc_u32 s15, s15, 0
	s_add_u32 s18, s18, 0x1000
	s_addc_u32 s19, s19, 0
	s_waitcnt vmcnt(45)
	v_cvt_pk_bf16_f32 v28, v24, v25
	v_cvt_pk_bf16_f32 v29, v26, v27
	v_fma_f32 v24, v36, v24, v32
	v_fma_f32 v25, v37, v25, v33
	v_fma_f32 v26, v38, v26, v34
	v_fma_f32 v27, v39, v27, v35
	global_store_dwordx2 v4, v[28:29], s[20:21]
	s_add_u32 s20, s20, 0x40000
	s_addc_u32 s21, s21, 0
	global_load_dwordx4 v[32:35], v3, s[14:15] nt
	global_load_dwordx4 v[36:39], v5, s[18:19]
	s_add_u32 s14, s14, 0x80000
	s_addc_u32 s15, s15, 0
	s_add_u32 s18, s18, 0x1000
	s_addc_u32 s19, s19, 0
	s_waitcnt vmcnt(45)
	v_cvt_pk_bf16_f32 v28, v24, v25
	v_cvt_pk_bf16_f32 v29, v26, v27
	v_fma_f32 v24, v44, v24, v40
	v_fma_f32 v25, v45, v25, v41
	v_fma_f32 v26, v46, v26, v42
	v_fma_f32 v27, v47, v27, v43
	global_store_dwordx2 v4, v[28:29], s[20:21]
	s_add_u32 s20, s20, 0x40000
	s_addc_u32 s21, s21, 0
	global_load_dwordx4 v[40:43], v3, s[14:15] nt
	global_load_dwordx4 v[44:47], v5, s[18:19]
	s_add_u32 s14, s14, 0x80000
	s_addc_u32 s15, s15, 0
	s_add_u32 s18, s18, 0x1000
	s_addc_u32 s19, s19, 0
	s_waitcnt vmcnt(45)
	v_cvt_pk_bf16_f32 v28, v24, v25
	v_cvt_pk_bf16_f32 v29, v26, v27
	v_fma_f32 v24, v52, v24, v48
	v_fma_f32 v25, v53, v25, v49
	v_fma_f32 v26, v54, v26, v50
	v_fma_f32 v27, v55, v27, v51
	global_store_dwordx2 v4, v[28:29], s[20:21]
	s_add_u32 s20, s20, 0x40000
	s_addc_u32 s21, s21, 0
	global_load_dwordx4 v[48:51], v3, s[14:15] nt
	global_load_dwordx4 v[52:55], v5, s[18:19]
	s_add_u32 s14, s14, 0x80000
	s_addc_u32 s15, s15, 0
	s_add_u32 s18, s18, 0x1000
	s_addc_u32 s19, s19, 0
	s_waitcnt vmcnt(45)
	v_cvt_pk_bf16_f32 v28, v24, v25
	v_cvt_pk_bf16_f32 v29, v26, v27
	v_fma_f32 v24, v60, v24, v56
	v_fma_f32 v25, v61, v25, v57
	v_fma_f32 v26, v62, v26, v58
	v_fma_f32 v27, v63, v27, v59
	global_store_dwordx2 v4, v[28:29], s[20:21]
	s_add_u32 s20, s20, 0x40000
	s_addc_u32 s21, s21, 0
	global_load_dwordx4 v[56:59], v3, s[14:15] nt
	global_load_dwordx4 v[60:63], v5, s[18:19]
	s_add_u32 s14, s14, 0x80000
	s_addc_u32 s15, s15, 0
	s_add_u32 s18, s18, 0x1000
	s_addc_u32 s19, s19, 0
	s_waitcnt vmcnt(45)
	v_cvt_pk_bf16_f32 v28, v24, v25
	v_cvt_pk_bf16_f32 v29, v26, v27
	v_fma_f32 v24, v76, v24, v72
	v_fma_f32 v25, v77, v25, v73
	v_fma_f32 v26, v78, v26, v74
	v_fma_f32 v27, v79, v27, v75
	global_store_dwordx2 v4, v[28:29], s[20:21]
	s_add_u32 s20, s20, 0x40000
	s_addc_u32 s21, s21, 0
	global_load_dwordx4 v[72:75], v3, s[14:15] nt
	global_load_dwordx4 v[76:79], v5, s[18:19]
	s_add_u32 s14, s14, 0x80000
	s_addc_u32 s15, s15, 0
	s_add_u32 s18, s18, 0x1000
	s_addc_u32 s19, s19, 0
	s_waitcnt vmcnt(45)
	v_cvt_pk_bf16_f32 v28, v24, v25
	v_cvt_pk_bf16_f32 v29, v26, v27
	v_fma_f32 v24, v84, v24, v80
	v_fma_f32 v25, v85, v25, v81
	v_fma_f32 v26, v86, v26, v82
	v_fma_f32 v27, v87, v27, v83
	global_store_dwordx2 v4, v[28:29], s[20:21]
	s_add_u32 s20, s20, 0x40000
	s_addc_u32 s21, s21, 0
	global_load_dwordx4 v[80:83], v3, s[14:15] nt
	global_load_dwordx4 v[84:87], v5, s[18:19]
	s_add_u32 s14, s14, 0x80000
	s_addc_u32 s15, s15, 0
	s_add_u32 s18, s18, 0x1000
	s_addc_u32 s19, s19, 0
	s_waitcnt vmcnt(45)
	v_cvt_pk_bf16_f32 v28, v24, v25
	v_cvt_pk_bf16_f32 v29, v26, v27
	v_fma_f32 v24, v92, v24, v88
	v_fma_f32 v25, v93, v25, v89
	v_fma_f32 v26, v94, v26, v90
	v_fma_f32 v27, v95, v27, v91
	global_store_dwordx2 v4, v[28:29], s[20:21]
	s_add_u32 s20, s20, 0x40000
	s_addc_u32 s21, s21, 0
	global_load_dwordx4 v[88:91], v3, s[14:15] nt
	global_load_dwordx4 v[92:95], v5, s[18:19]
	s_add_u32 s14, s14, 0x80000
	s_addc_u32 s15, s15, 0
	s_add_u32 s18, s18, 0x1000
	s_addc_u32 s19, s19, 0
	s_waitcnt vmcnt(45)
	v_cvt_pk_bf16_f32 v28, v24, v25
	v_cvt_pk_bf16_f32 v29, v26, v27
	v_fma_f32 v24, v104, v24, v100
	v_fma_f32 v25, v105, v25, v101
	v_fma_f32 v26, v106, v26, v102
	v_fma_f32 v27, v107, v27, v103
	global_store_dwordx2 v4, v[28:29], s[20:21]
	s_add_u32 s20, s20, 0x40000
	s_addc_u32 s21, s21, 0
	global_load_dwordx4 v[100:103], v3, s[14:15] nt
	global_load_dwordx4 v[104:107], v5, s[18:19]
	s_add_u32 s14, s14, 0x80000
	s_addc_u32 s15, s15, 0
	s_add_u32 s18, s18, 0x1000
	s_addc_u32 s19, s19, 0
	s_waitcnt vmcnt(45)
; #define H2_LOAD(V, D, C0) do { _Pragma("unroll") for (int u = 0; u < 6; ++u) { V[u] = __builtin_nontemporal_load(kv + (size_t)((C0) + u) * 8 * 16384); D[u] = dc[(size_t)((C0) + u) * 8 * 128]; } } while (0)
; #define H2_STEP(V, D, C0) do { _Pragma("unroll") for (int u = 0; u < 6; ++u) { sb[(size_t)((C0) + u) * 8 * 16384] = f2bf(S); S = fmaf(D[u], S, V[u]); } } while (0)
; __device__ __forceinline__ void ph_hgrn_chain2(const P& p, int gt, int nt) {
;     ...
;     H2_LOAD(a, da, 0);
; #pragma unroll 1
;     for (int c0 = 0; c0 < HG_NCH; c0 += 12) {
;       H2_LOAD(b2, db, c0 + 6); H2_STEP(a, da, c0);
;       if (c0 + 12 < HG_NCH) H2_LOAD(a, da, c0 + 12);
;       H2_STEP(b2, db, c0 + 6);
	v_cvt_pk_bf16_f32 v28, v24, v25
	v_cvt_pk_bf16_f32 v29, v26, v27
	v_fma_f32 v24, v112, v24, v108
	v_fma_f32 v25, v113, v25, v109
	v_fma_f32 v26, v114, v26, v110
	v_fma_f32 v27, v115, v27, v111
	global_store_dwordx2 v4, v[28:29], s[20:21]
	s_add_u32 s20, s20, 0x40000
	s_addc_u32 s21, s21, 0
	global_load_dwordx4 v[108:111], v3, s[14:15] nt
	global_load_dwordx4 v[112:115], v5, s[18:19]
	s_add_u32 s14, s14, 0x80000
	s_addc_u32 s15, s15, 0
	s_add_u32 s18, s18, 0x1000
	s_addc_u32 s19, s19, 0
	s_waitcnt vmcnt(45)
	v_cvt_pk_bf16_f32 v28, v24, v25
	v_cvt_pk_bf16_f32 v29, v26, v27
	v_fma_f32 v24, v120, v24, v116
	v_fma_f32 v25, v121, v25, v117
	v_fma_f32 v26, v122, v26, v118
	v_fma_f32 v27, v123, v27, v119
	global_store_dwordx2 v4, v[28:29], s[20:21]
	s_add_u32 s20, s20, 0x40000
	s_addc_u32 s21, s21, 0
	global_load_dwordx4 v[116:119], v3, s[14:15] nt
	global_load_dwordx4 v[120:123], v5, s[18:19]
	s_add_u32 s14, s14, 0x80000
	s_addc_u32 s15, s15, 0
	s_add_u32 s18, s18, 0x1000
	s_addc_u32 s19, s19, 0
	s_waitcnt vmcnt(45)
	v_cvt_pk_bf16_f32 v28, v24, v25
	v_cvt_pk_bf16_f32 v29, v26, v27
	v_fma_f32 v24, v128, v24, v124
	v_fma_f32 v25, v129, v25, v125
	v_fma_f32 v26, v130, v26, v126
	v_fma_f32 v27, v131, v27, v127
	global_store_dwordx2 v4, v[28:29], s[20:21]
	s_add_u32 s20, s20, 0x40000
	s_addc_u32 s21, s21, 0
	global_load_dwordx4 v[124:127], v3, s[14:15] nt
	global_load_dwordx4 v[128:131], v5, s[18:19]
	s_add_u32 s14, s14, 0x80000
	s_addc_u32 s15, s15, 0
	s_add_u32 s18, s18, 0x1000
	s_addc_u32 s19, s19, 0
	s_waitcnt vmcnt(45)
	v_cvt_pk_bf16_f32 v28, v24, v25
	v_cvt_pk_bf16_f32 v29, v26, v27
	v_fma_f32 v24, v136, v24, v132
	v_fma_f32 v25, v137, v25, v133
	v_fma_f32 v26, v138, v26, v134
	v_fma_f32 v27, v139, v27, v135
	global_store_dwordx2 v4, v[28:29], s[20:21]
	s_add_u32 s20, s20, 0x40000
	s_addc_u32 s21, s21, 0
	global_load_dwordx4 v[132:135], v3, s[14:15] nt
	global_load_dwordx4 v[136:139], v5, s[18:19]
	s_add_u32 s14, s14, 0x80000
	s_addc_u32 s15, s15, 0
	s_add_u32 s18, s18, 0x1000
	s_addc_u32 s19, s19, 0
	s_waitcnt vmcnt(45)
	v_cvt_pk_bf16_f32 v28, v24, v25
	v_cvt_pk_bf16_f32 v29, v26, v27
	v_fma_f32 v24, v144, v24, v140
	v_fma_f32 v25, v145, v25, v141
	v_fma_f32 v26, v146, v26, v142
	v_fma_f32 v27, v147, v27, v143
	global_store_dwordx2 v4, v[28:29], s[20:21]
	s_add_u32 s20, s20, 0x40000
	s_addc_u32 s21, s21, 0
	global_load_dwordx4 v[140:143], v3, s[14:15] nt
	global_load_dwordx4 v[144:147], v5, s[18:19]
	s_add_u32 s14, s14, 0x80000
	s_addc_u32 s15, s15, 0
	s_add_u32 s18, s18, 0x1000
	s_addc_u32 s19, s19, 0
	s_waitcnt vmcnt(45)
	v_cvt_pk_bf16_f32 v28, v24, v25
	v_cvt_pk_bf16_f32 v29, v26, v27
	v_fma_f32 v24, v152, v24, v148
	v_fma_f32 v25, v153, v25, v149
	v_fma_f32 v26, v154, v26, v150
	v_fma_f32 v27, v155, v27, v151
	global_store_dwordx2 v4, v[28:29], s[20:21]
	s_add_u32 s20, s20, 0x40000
	s_addc_u32 s21, s21, 0
	global_load_dwordx4 v[148:151], v3, s[14:15] nt
	global_load_dwordx4 v[152:155], v5, s[18:19]
	s_add_u32 s14, s14, 0x80000
	s_addc_u32 s15, s15, 0
	s_add_u32 s18, s18, 0x1000
	s_addc_u32 s19, s19, 0
	s_waitcnt vmcnt(45)
	v_cvt_pk_bf16_f32 v28, v24, v25
	v_cvt_pk_bf16_f32 v29, v26, v27
	v_fma_f32 v24, v160, v24, v156
	v_fma_f32 v25, v161, v25, v157
	v_fma_f32 v26, v162, v26, v158
	v_fma_f32 v27, v163, v27, v159
	global_store_dwordx2 v4, v[28:29], s[20:21]
	s_add_u32 s20, s20, 0x40000
	s_addc_u32 s21, s21, 0
	global_load_dwordx4 v[156:159], v3, s[14:15] nt
	global_load_dwordx4 v[160:163], v5, s[18:19]
	s_add_u32 s14, s14, 0x80000
	s_addc_u32 s15, s15, 0
	s_add_u32 s18, s18, 0x1000
	s_addc_u32 s19, s19, 0
	s_waitcnt vmcnt(45)
	v_cvt_pk_bf16_f32 v28, v24, v25
	v_cvt_pk_bf16_f32 v29, v26, v27
	v_fma_f32 v24, v168, v24, v164
	v_fma_f32 v25, v169, v25, v165
	v_fma_f32 v26, v170, v26, v166
	v_fma_f32 v27, v171, v27, v167
	global_store_dwordx2 v4, v[28:29], s[20:21]
	s_add_u32 s20, s20, 0x40000
	s_addc_u32 s21, s21, 0
	global_load_dwordx4 v[164:167], v3, s[14:15] nt
	global_load_dwordx4 v[168:171], v5, s[18:19]
	s_add_u32 s14, s14, 0x80000
	s_addc_u32 s15, s15, 0
	s_add_u32 s18, s18, 0x1000
	s_addc_u32 s19, s19, 0
	s_waitcnt vmcnt(45)
	v_cvt_pk_bf16_f32 v28, v24, v25
	v_cvt_pk_bf16_f32 v29, v26, v27
	v_fma_f32 v24, v36, v24, v32
	v_fma_f32 v25, v37, v25, v33
	v_fma_f32 v26, v38, v26, v34
	v_fma_f32 v27, v39, v27, v35
	global_store_dwordx2 v4, v[28:29], s[20:21]
	s_add_u32 s20, s20, 0x40000
	s_addc_u32 s21, s21, 0
	global_load_dwordx4 v[32:35], v3, s[14:15] nt
	global_load_dwordx4 v[36:39], v5, s[18:19]
	s_add_u32 s14, s14, 0x80000
	s_addc_u32 s15, s15, 0
	s_add_u32 s18, s18, 0x1000
	s_addc_u32 s19, s19, 0
	s_waitcnt vmcnt(45)
	v_cvt_pk_bf16_f32 v28, v24, v25
	v_cvt_pk_bf16_f32 v29, v26, v27
	v_fma_f32 v24, v44, v24, v40
	v_fma_f32 v25, v45, v25, v41
	v_fma_f32 v26, v46, v26, v42
	v_fma_f32 v27, v47, v27, v43
	global_store_dwordx2 v4, v[28:29], s[20:21]
	s_add_u32 s20, s20, 0x40000
	s_addc_u32 s21, s21, 0
	global_load_dwordx4 v[40:43], v3, s[14:15] nt
	global_load_dwordx4 v[44:47], v5, s[18:19]
	s_add_u32 s14, s14, 0x80000
	s_addc_u32 s15, s15, 0
	s_add_u32 s18, s18, 0x1000
	s_addc_u32 s19, s19, 0
	s_waitcnt vmcnt(45)
	v_cvt_pk_bf16_f32 v28, v24, v25
	v_cvt_pk_bf16_f32 v29, v26, v27
	v_fma_f32 v24, v52, v24, v48
	v_fma_f32 v25, v53, v25, v49
	v_fma_f32 v26, v54, v26, v50
	v_fma_f32 v27, v55, v27, v51
	global_store_dwordx2 v4, v[28:29], s[20:21]
	s_add_u32 s20, s20, 0x40000
	s_addc_u32 s21, s21, 0
	global_load_dwordx4 v[48:51], v3, s[14:15] nt
	global_load_dwordx4 v[52:55], v5, s[18:19]
	s_add_u32 s14, s14, 0x80000
	s_addc_u32 s15, s15, 0
	s_add_u32 s18, s18, 0x1000
	s_addc_u32 s19, s19, 0
	s_waitcnt vmcnt(45)
; #define H2_LOAD(V, D, C0) do { _Pragma("unroll") for (int u = 0; u < 6; ++u) { V[u] = __builtin_nontemporal_load(kv + (size_t)((C0) + u) * 8 * 16384); D[u] = dc[(size_t)((C0) + u) * 8 * 128]; } } while (0)
; #define H2_STEP(V, D, C0) do { _Pragma("unroll") for (int u = 0; u < 6; ++u) { sb[(size_t)((C0) + u) * 8 * 16384] = f2bf(S); S = fmaf(D[u], S, V[u]); } } while (0)
; __device__ __forceinline__ void ph_hgrn_chain2(const P& p, int gt, int nt) {
;     ...
;     H2_LOAD(a, da, 0);
; #pragma unroll 1
;     for (int c0 = 0; c0 < HG_NCH; c0 += 12) {
;       H2_LOAD(b2, db, c0 + 6); H2_STEP(a, da, c0);
;       if (c0 + 12 < HG_NCH) H2_LOAD(a, da, c0 + 12);
;       H2_STEP(b2, db, c0 + 6);
	v_cvt_pk_bf16_f32 v28, v24, v25
	v_cvt_pk_bf16_f32 v29, v26, v27
	v_fma_f32 v24, v60, v24, v56
	v_fma_f32 v25, v61, v25, v57
	v_fma_f32 v26, v62, v26, v58
	v_fma_f32 v27, v63, v27, v59
	global_store_dwordx2 v4, v[28:29], s[20:21]
	s_add_u32 s20, s20, 0x40000
	s_addc_u32 s21, s21, 0
	global_load_dwordx4 v[56:59], v3, s[14:15] nt
	global_load_dwordx4 v[60:63], v5, s[18:19]
	s_add_u32 s14, s14, 0x80000
	s_addc_u32 s15, s15, 0
	s_add_u32 s18, s18, 0x1000
	s_addc_u32 s19, s19, 0
	s_waitcnt vmcnt(45)
	v_cvt_pk_bf16_f32 v28, v24, v25
	v_cvt_pk_bf16_f32 v29, v26, v27
	v_fma_f32 v24, v76, v24, v72
	v_fma_f32 v25, v77, v25, v73
	v_fma_f32 v26, v78, v26, v74
	v_fma_f32 v27, v79, v27, v75
	global_store_dwordx2 v4, v[28:29], s[20:21]
	s_add_u32 s20, s20, 0x40000
	s_addc_u32 s21, s21, 0
	global_load_dwordx4 v[72:75], v3, s[14:15] nt
	global_load_dwordx4 v[76:79], v5, s[18:19]
	s_add_u32 s14, s14, 0x80000
	s_addc_u32 s15, s15, 0
	s_add_u32 s18, s18, 0x1000
	s_addc_u32 s19, s19, 0
	s_waitcnt vmcnt(45)
	v_cvt_pk_bf16_f32 v28, v24, v25
	v_cvt_pk_bf16_f32 v29, v26, v27
	v_fma_f32 v24, v84, v24, v80
	v_fma_f32 v25, v85, v25, v81
	v_fma_f32 v26, v86, v26, v82
	v_fma_f32 v27, v87, v27, v83
	global_store_dwordx2 v4, v[28:29], s[20:21]
	s_add_u32 s20, s20, 0x40000
	s_addc_u32 s21, s21, 0
	global_load_dwordx4 v[80:83], v3, s[14:15] nt
	global_load_dwordx4 v[84:87], v5, s[18:19]
	s_add_u32 s14, s14, 0x80000
	s_addc_u32 s15, s15, 0
	s_add_u32 s18, s18, 0x1000
	s_addc_u32 s19, s19, 0
	s_waitcnt vmcnt(45)
	v_cvt_pk_bf16_f32 v28, v24, v25
	v_cvt_pk_bf16_f32 v29, v26, v27
	v_fma_f32 v24, v92, v24, v88
	v_fma_f32 v25, v93, v25, v89
	v_fma_f32 v26, v94, v26, v90
	v_fma_f32 v27, v95, v27, v91
	global_store_dwordx2 v4, v[28:29], s[20:21]
	s_add_u32 s20, s20, 0x40000
	s_addc_u32 s21, s21, 0
	global_load_dwordx4 v[88:91], v3, s[14:15] nt
	global_load_dwordx4 v[92:95], v5, s[18:19]
	s_add_u32 s14, s14, 0x80000
	s_addc_u32 s15, s15, 0
	s_add_u32 s18, s18, 0x1000
	s_addc_u32 s19, s19, 0
	s_waitcnt vmcnt(45)
	v_cvt_pk_bf16_f32 v28, v24, v25
	v_cvt_pk_bf16_f32 v29, v26, v27
	v_fma_f32 v24, v104, v24, v100
	v_fma_f32 v25, v105, v25, v101
	v_fma_f32 v26, v106, v26, v102
	v_fma_f32 v27, v107, v27, v103
	global_store_dwordx2 v4, v[28:29], s[20:21]
	s_add_u32 s20, s20, 0x40000
	s_addc_u32 s21, s21, 0
	global_load_dwordx4 v[100:103], v3, s[14:15] nt
	global_load_dwordx4 v[104:107], v5, s[18:19]
	s_add_u32 s14, s14, 0x80000
	s_addc_u32 s15, s15, 0
	s_add_u32 s18, s18, 0x1000
	s_addc_u32 s19, s19, 0
	s_waitcnt vmcnt(45)
	v_cvt_pk_bf16_f32 v28, v24, v25
	v_cvt_pk_bf16_f32 v29, v26, v27
	v_fma_f32 v24, v112, v24, v108
	v_fma_f32 v25, v113, v25, v109
	v_fma_f32 v26, v114, v26, v110
	v_fma_f32 v27, v115, v27, v111
	global_store_dwordx2 v4, v[28:29], s[20:21]
	s_add_u32 s20, s20, 0x40000
	s_addc_u32 s21, s21, 0
	global_load_dwordx4 v[108:111], v3, s[14:15] nt
	global_load_dwordx4 v[112:115], v5, s[18:19]
	s_add_u32 s14, s14, 0x80000
	s_addc_u32 s15, s15, 0
	s_add_u32 s18, s18, 0x1000
	s_addc_u32 s19, s19, 0
	s_waitcnt vmcnt(45)
	v_cvt_pk_bf16_f32 v28, v24, v25
	v_cvt_pk_bf16_f32 v29, v26, v27
	v_fma_f32 v24, v120, v24, v116
	v_fma_f32 v25, v121, v25, v117
	v_fma_f32 v26, v122, v26, v118
	v_fma_f32 v27, v123, v27, v119
	global_store_dwordx2 v4, v[28:29], s[20:21]
	s_add_u32 s20, s20, 0x40000
	s_addc_u32 s21, s21, 0
	global_load_dwordx4 v[116:119], v3, s[14:15] nt
	global_load_dwordx4 v[120:123], v5, s[18:19]
	s_add_u32 s14, s14, 0x80000
	s_addc_u32 s15, s15, 0
	s_add_u32 s18, s18, 0x1000
	s_addc_u32 s19, s19, 0
	s_waitcnt vmcnt(45)
	v_cvt_pk_bf16_f32 v28, v24, v25
	v_cvt_pk_bf16_f32 v29, v26, v27
	v_fma_f32 v24, v128, v24, v124
	v_fma_f32 v25, v129, v25, v125
	v_fma_f32 v26, v130, v26, v126
	v_fma_f32 v27, v131, v27, v127
	global_store_dwordx2 v4, v[28:29], s[20:21]
	s_add_u32 s20, s20, 0x40000
	s_addc_u32 s21, s21, 0
	global_load_dwordx4 v[124:127], v3, s[14:15] nt
	global_load_dwordx4 v[128:131], v5, s[18:19]
	s_add_u32 s14, s14, 0x80000
	s_addc_u32 s15, s15, 0
	s_add_u32 s18, s18, 0x1000
	s_addc_u32 s19, s19, 0
	s_waitcnt vmcnt(45)
	v_cvt_pk_bf16_f32 v28, v24, v25
	v_cvt_pk_bf16_f32 v29, v26, v27
	v_fma_f32 v24, v136, v24, v132
	v_fma_f32 v25, v137, v25, v133
	v_fma_f32 v26, v138, v26, v134
	v_fma_f32 v27, v139, v27, v135
	global_store_dwordx2 v4, v[28:29], s[20:21]
	s_add_u32 s20, s20, 0x40000
	s_addc_u32 s21, s21, 0
	global_load_dwordx4 v[132:135], v3, s[14:15] nt
	global_load_dwordx4 v[136:139], v5, s[18:19]
	s_add_u32 s14, s14, 0x80000
	s_addc_u32 s15, s15, 0
	s_add_u32 s18, s18, 0x1000
	s_addc_u32 s19, s19, 0
	s_waitcnt vmcnt(45)
	v_cvt_pk_bf16_f32 v28, v24, v25
	v_cvt_pk_bf16_f32 v29, v26, v27
	v_fma_f32 v24, v144, v24, v140
	v_fma_f32 v25, v145, v25, v141
	v_fma_f32 v26, v146, v26, v142
	v_fma_f32 v27, v147, v27, v143
	global_store_dwordx2 v4, v[28:29], s[20:21]
	s_add_u32 s20, s20, 0x40000
	s_addc_u32 s21, s21, 0
	global_load_dwordx4 v[140:143], v3, s[14:15] nt
	global_load_dwordx4 v[144:147], v5, s[18:19]
	s_add_u32 s14, s14, 0x80000
	s_addc_u32 s15, s15, 0
	s_add_u32 s18, s18, 0x1000
	s_addc_u32 s19, s19, 0
	s_waitcnt vmcnt(45)
	v_cvt_pk_bf16_f32 v28, v24, v25
	v_cvt_pk_bf16_f32 v29, v26, v27
	v_fma_f32 v24, v152, v24, v148
	v_fma_f32 v25, v153, v25, v149
	v_fma_f32 v26, v154, v26, v150
	v_fma_f32 v27, v155, v27, v151
	global_store_dwordx2 v4, v[28:29], s[20:21]
	s_add_u32 s20, s20, 0x40000
	s_addc_u32 s21, s21, 0
	global_load_dwordx4 v[148:151], v3, s[14:15] nt
	global_load_dwordx4 v[152:155], v5, s[18:19]
	s_add_u32 s14, s14, 0x80000
	s_addc_u32 s15, s15, 0
	s_add_u32 s18, s18, 0x1000
	s_addc_u32 s19, s19, 0
	s_waitcnt vmcnt(45)
; #define H2_LOAD(V, D, C0) do { _Pragma("unroll") for (int u = 0; u < 6; ++u) { V[u] = __builtin_nontemporal_load(kv + (size_t)((C0) + u) * 8 * 16384); D[u] = dc[(size_t)((C0) + u) * 8 * 128]; } } while (0)
; #define H2_STEP(V, D, C0) do { _Pragma("unroll") for (int u = 0; u < 6; ++u) { sb[(size_t)((C0) + u) * 8 * 16384] = f2bf(S); S = fmaf(D[u], S, V[u]); } } while (0)
; __device__ __forceinline__ void ph_hgrn_chain2(const P& p, int gt, int nt) {
;     ...
;     H2_LOAD(a, da, 0);
; #pragma unroll 1
;     for (int c0 = 0; c0 < HG_NCH; c0 += 12) {
;       H2_LOAD(b2, db, c0 + 6); H2_STEP(a, da, c0);
;       if (c0 + 12 < HG_NCH) H2_LOAD(a, da, c0 + 12);
;       H2_STEP(b2, db, c0 + 6);
	v_cvt_pk_bf16_f32 v28, v24, v25
	v_cvt_pk_bf16_f32 v29, v26, v27
	v_fma_f32 v24, v160, v24, v156
	v_fma_f32 v25, v161, v25, v157
	v_fma_f32 v26, v162, v26, v158
	v_fma_f32 v27, v163, v27, v159
	global_store_dwordx2 v4, v[28:29], s[20:21]
	s_add_u32 s20, s20, 0x40000
	s_addc_u32 s21, s21, 0
	global_load_dwordx4 v[156:159], v3, s[14:15] nt
	global_load_dwordx4 v[160:163], v5, s[18:19]
	s_add_u32 s14, s14, 0x80000
	s_addc_u32 s15, s15, 0
	s_add_u32 s18, s18, 0x1000
	s_addc_u32 s19, s19, 0
	s_waitcnt vmcnt(45)
	v_cvt_pk_bf16_f32 v28, v24, v25
	v_cvt_pk_bf16_f32 v29, v26, v27
	v_fma_f32 v24, v168, v24, v164
	v_fma_f32 v25, v169, v25, v165
	v_fma_f32 v26, v170, v26, v166
	v_fma_f32 v27, v171, v27, v167
	global_store_dwordx2 v4, v[28:29], s[20:21]
	s_add_u32 s20, s20, 0x40000
	s_addc_u32 s21, s21, 0
	global_load_dwordx4 v[164:167], v3, s[14:15] nt
	global_load_dwordx4 v[168:171], v5, s[18:19]
	s_add_u32 s14, s14, 0x80000
	s_addc_u32 s15, s15, 0
	s_add_u32 s18, s18, 0x1000
	s_addc_u32 s19, s19, 0
	s_waitcnt vmcnt(45)
	v_cvt_pk_bf16_f32 v28, v24, v25
	v_cvt_pk_bf16_f32 v29, v26, v27
	v_fma_f32 v24, v36, v24, v32
	v_fma_f32 v25, v37, v25, v33
	v_fma_f32 v26, v38, v26, v34
	v_fma_f32 v27, v39, v27, v35
	global_store_dwordx2 v4, v[28:29], s[20:21]
	s_add_u32 s20, s20, 0x40000
	s_addc_u32 s21, s21, 0
	global_load_dwordx4 v[32:35], v3, s[14:15] nt
	global_load_dwordx4 v[36:39], v5, s[18:19]
	s_add_u32 s14, s14, 0x80000
	s_addc_u32 s15, s15, 0
	s_add_u32 s18, s18, 0x1000
	s_addc_u32 s19, s19, 0
	s_waitcnt vmcnt(45)
	v_cvt_pk_bf16_f32 v28, v24, v25
	v_cvt_pk_bf16_f32 v29, v26, v27
	v_fma_f32 v24, v44, v24, v40
	v_fma_f32 v25, v45, v25, v41
	v_fma_f32 v26, v46, v26, v42
	v_fma_f32 v27, v47, v27, v43
	global_store_dwordx2 v4, v[28:29], s[20:21]
	s_add_u32 s20, s20, 0x40000
	s_addc_u32 s21, s21, 0
	global_load_dwordx4 v[40:43], v3, s[14:15] nt
	global_load_dwordx4 v[44:47], v5, s[18:19]
	s_add_u32 s14, s14, 0x80000
	s_addc_u32 s15, s15, 0
	s_add_u32 s18, s18, 0x1000
	s_addc_u32 s19, s19, 0
	s_waitcnt vmcnt(45)
	v_cvt_pk_bf16_f32 v28, v24, v25
	v_cvt_pk_bf16_f32 v29, v26, v27
	v_fma_f32 v24, v52, v24, v48
	v_fma_f32 v25, v53, v25, v49
	v_fma_f32 v26, v54, v26, v50
	v_fma_f32 v27, v55, v27, v51
	global_store_dwordx2 v4, v[28:29], s[20:21]
	s_add_u32 s20, s20, 0x40000
	s_addc_u32 s21, s21, 0
	global_load_dwordx4 v[48:51], v3, s[14:15] nt
	global_load_dwordx4 v[52:55], v5, s[18:19]
	s_add_u32 s14, s14, 0x80000
	s_addc_u32 s15, s15, 0
	s_add_u32 s18, s18, 0x1000
	s_addc_u32 s19, s19, 0
	s_waitcnt vmcnt(45)
	v_cvt_pk_bf16_f32 v28, v24, v25
	v_cvt_pk_bf16_f32 v29, v26, v27
	v_fma_f32 v24, v60, v24, v56
	v_fma_f32 v25, v61, v25, v57
	v_fma_f32 v26, v62, v26, v58
	v_fma_f32 v27, v63, v27, v59
	global_store_dwordx2 v4, v[28:29], s[20:21]
	s_add_u32 s20, s20, 0x40000
	s_addc_u32 s21, s21, 0
	global_load_dwordx4 v[56:59], v3, s[14:15] nt
	global_load_dwordx4 v[60:63], v5, s[18:19]
	s_add_u32 s14, s14, 0x80000
	s_addc_u32 s15, s15, 0
	s_add_u32 s18, s18, 0x1000
	s_addc_u32 s19, s19, 0
	s_waitcnt vmcnt(45)
	v_cvt_pk_bf16_f32 v28, v24, v25
	v_cvt_pk_bf16_f32 v29, v26, v27
	v_fma_f32 v24, v76, v24, v72
	v_fma_f32 v25, v77, v25, v73
	v_fma_f32 v26, v78, v26, v74
	v_fma_f32 v27, v79, v27, v75
	global_store_dwordx2 v4, v[28:29], s[20:21]
	s_add_u32 s20, s20, 0x40000
	s_addc_u32 s21, s21, 0
	global_load_dwordx4 v[72:75], v3, s[14:15] nt
	global_load_dwordx4 v[76:79], v5, s[18:19]
	s_add_u32 s14, s14, 0x80000
	s_addc_u32 s15, s15, 0
	s_add_u32 s18, s18, 0x1000
	s_addc_u32 s19, s19, 0
	s_waitcnt vmcnt(45)
	v_cvt_pk_bf16_f32 v28, v24, v25
	v_cvt_pk_bf16_f32 v29, v26, v27
	v_fma_f32 v24, v84, v24, v80
	v_fma_f32 v25, v85, v25, v81
	v_fma_f32 v26, v86, v26, v82
	v_fma_f32 v27, v87, v27, v83
	global_store_dwordx2 v4, v[28:29], s[20:21]
	s_add_u32 s20, s20, 0x40000
	s_addc_u32 s21, s21, 0
	global_load_dwordx4 v[80:83], v3, s[14:15] nt
	global_load_dwordx4 v[84:87], v5, s[18:19]
	s_add_u32 s14, s14, 0x80000
	s_addc_u32 s15, s15, 0
	s_add_u32 s18, s18, 0x1000
	s_addc_u32 s19, s19, 0
	s_waitcnt vmcnt(45)
	v_cvt_pk_bf16_f32 v28, v24, v25
	v_cvt_pk_bf16_f32 v29, v26, v27
	v_fma_f32 v24, v92, v24, v88
	v_fma_f32 v25, v93, v25, v89
	v_fma_f32 v26, v94, v26, v90
	v_fma_f32 v27, v95, v27, v91
	global_store_dwordx2 v4, v[28:29], s[20:21]
	s_add_u32 s20, s20, 0x40000
	s_addc_u32 s21, s21, 0
	global_load_dwordx4 v[88:91], v3, s[14:15] nt
	global_load_dwordx4 v[92:95], v5, s[18:19]
	s_add_u32 s14, s14, 0x80000
	s_addc_u32 s15, s15, 0
	s_add_u32 s18, s18, 0x1000
	s_addc_u32 s19, s19, 0
	s_waitcnt vmcnt(45)
	v_cvt_pk_bf16_f32 v28, v24, v25
	v_cvt_pk_bf16_f32 v29, v26, v27
	v_fma_f32 v24, v104, v24, v100
	v_fma_f32 v25, v105, v25, v101
	v_fma_f32 v26, v106, v26, v102
	v_fma_f32 v27, v107, v27, v103
	global_store_dwordx2 v4, v[28:29], s[20:21]
	s_add_u32 s20, s20, 0x40000
	s_addc_u32 s21, s21, 0
	global_load_dwordx4 v[100:103], v3, s[14:15] nt
	global_load_dwordx4 v[104:107], v5, s[18:19]
	s_add_u32 s14, s14, 0x80000
	s_addc_u32 s15, s15, 0
	s_add_u32 s18, s18, 0x1000
	s_addc_u32 s19, s19, 0
	s_waitcnt vmcnt(45)
	v_cvt_pk_bf16_f32 v28, v24, v25
	v_cvt_pk_bf16_f32 v29, v26, v27
	v_fma_f32 v24, v112, v24, v108
	v_fma_f32 v25, v113, v25, v109
	v_fma_f32 v26, v114, v26, v110
	v_fma_f32 v27, v115, v27, v111
	global_store_dwordx2 v4, v[28:29], s[20:21]
	s_add_u32 s20, s20, 0x40000
	s_addc_u32 s21, s21, 0
	global_load_dwordx4 v[108:111], v3, s[14:15] nt
	global_load_dwordx4 v[112:115], v5, s[18:19]
	s_add_u32 s14, s14, 0x80000
	s_addc_u32 s15, s15, 0
	s_add_u32 s18, s18, 0x1000
	s_addc_u32 s19, s19, 0
	s_waitcnt vmcnt(45)
; #define H2_LOAD(V, D, C0) do { _Pragma("unroll") for (int u = 0; u < 6; ++u) { V[u] = __builtin_nontemporal_load(kv + (size_t)((C0) + u) * 8 * 16384); D[u] = dc[(size_t)((C0) + u) * 8 * 128]; } } while (0)
; #define H2_STEP(V, D, C0) do { _Pragma("unroll") for (int u = 0; u < 6; ++u) { sb[(size_t)((C0) + u) * 8 * 16384] = f2bf(S); S = fmaf(D[u], S, V[u]); } } while (0)
; __device__ __forceinline__ void ph_hgrn_chain2(const P& p, int gt, int nt) {
;     ...
;     H2_LOAD(a, da, 0);
; #pragma unroll 1
;     for (int c0 = 0; c0 < HG_NCH; c0 += 12) {
;       H2_LOAD(b2, db, c0 + 6); H2_STEP(a, da, c0);
;       if (c0 + 12 < HG_NCH) H2_LOAD(a, da, c0 + 12);
;       H2_STEP(b2, db, c0 + 6);
	v_cvt_pk_bf16_f32 v28, v24, v25
	v_cvt_pk_bf16_f32 v29, v26, v27
	v_fma_f32 v24, v120, v24, v116
	v_fma_f32 v25, v121, v25, v117
	v_fma_f32 v26, v122, v26, v118
	v_fma_f32 v27, v123, v27, v119
	global_store_dwordx2 v4, v[28:29], s[20:21]
	s_add_u32 s20, s20, 0x40000
	s_addc_u32 s21, s21, 0
	global_load_dwordx4 v[116:119], v3, s[14:15] nt
	global_load_dwordx4 v[120:123], v5, s[18:19]
	s_add_u32 s14, s14, 0x80000
	s_addc_u32 s15, s15, 0
	s_add_u32 s18, s18, 0x1000
	s_addc_u32 s19, s19, 0
	s_waitcnt vmcnt(45)
	v_cvt_pk_bf16_f32 v28, v24, v25
	v_cvt_pk_bf16_f32 v29, v26, v27
	v_fma_f32 v24, v128, v24, v124
	v_fma_f32 v25, v129, v25, v125
	v_fma_f32 v26, v130, v26, v126
	v_fma_f32 v27, v131, v27, v127
	global_store_dwordx2 v4, v[28:29], s[20:21]
	s_add_u32 s20, s20, 0x40000
	s_addc_u32 s21, s21, 0
	global_load_dwordx4 v[124:127], v3, s[14:15] nt
	global_load_dwordx4 v[128:131], v5, s[18:19]
	s_add_u32 s14, s14, 0x80000
	s_addc_u32 s15, s15, 0
	s_add_u32 s18, s18, 0x1000
	s_addc_u32 s19, s19, 0
	s_waitcnt vmcnt(45)
	v_cvt_pk_bf16_f32 v28, v24, v25
	v_cvt_pk_bf16_f32 v29, v26, v27
	v_fma_f32 v24, v136, v24, v132
	v_fma_f32 v25, v137, v25, v133
	v_fma_f32 v26, v138, v26, v134
	v_fma_f32 v27, v139, v27, v135
	global_store_dwordx2 v4, v[28:29], s[20:21]
	s_add_u32 s20, s20, 0x40000
	s_addc_u32 s21, s21, 0
	global_load_dwordx4 v[132:135], v3, s[14:15] nt
	global_load_dwordx4 v[136:139], v5, s[18:19]
	s_add_u32 s14, s14, 0x80000
	s_addc_u32 s15, s15, 0
	s_add_u32 s18, s18, 0x1000
	s_addc_u32 s19, s19, 0
	s_waitcnt vmcnt(45)
	v_cvt_pk_bf16_f32 v28, v24, v25
	v_cvt_pk_bf16_f32 v29, v26, v27
	v_fma_f32 v24, v144, v24, v140
	v_fma_f32 v25, v145, v25, v141
	v_fma_f32 v26, v146, v26, v142
	v_fma_f32 v27, v147, v27, v143
	global_store_dwordx2 v4, v[28:29], s[20:21]
	s_add_u32 s20, s20, 0x40000
	s_addc_u32 s21, s21, 0
	global_load_dwordx4 v[140:143], v3, s[14:15] nt
	global_load_dwordx4 v[144:147], v5, s[18:19]
	s_add_u32 s14, s14, 0x80000
	s_addc_u32 s15, s15, 0
	s_add_u32 s18, s18, 0x1000
	s_addc_u32 s19, s19, 0
	s_waitcnt vmcnt(45)
	v_cvt_pk_bf16_f32 v28, v24, v25
	v_cvt_pk_bf16_f32 v29, v26, v27
	v_fma_f32 v24, v152, v24, v148
	v_fma_f32 v25, v153, v25, v149
	v_fma_f32 v26, v154, v26, v150
	v_fma_f32 v27, v155, v27, v151
	global_store_dwordx2 v4, v[28:29], s[20:21]
	s_add_u32 s20, s20, 0x40000
	s_addc_u32 s21, s21, 0
	global_load_dwordx4 v[148:151], v3, s[14:15] nt
	global_load_dwordx4 v[152:155], v5, s[18:19]
	s_add_u32 s14, s14, 0x80000
	s_addc_u32 s15, s15, 0
	s_add_u32 s18, s18, 0x1000
	s_addc_u32 s19, s19, 0
	s_waitcnt vmcnt(45)
	v_cvt_pk_bf16_f32 v28, v24, v25
	v_cvt_pk_bf16_f32 v29, v26, v27
	v_fma_f32 v24, v160, v24, v156
	v_fma_f32 v25, v161, v25, v157
	v_fma_f32 v26, v162, v26, v158
	v_fma_f32 v27, v163, v27, v159
	global_store_dwordx2 v4, v[28:29], s[20:21]
	s_add_u32 s20, s20, 0x40000
	s_addc_u32 s21, s21, 0
	global_load_dwordx4 v[156:159], v3, s[14:15] nt
	global_load_dwordx4 v[160:163], v5, s[18:19]
	s_add_u32 s14, s14, 0x80000
	s_addc_u32 s15, s15, 0
	s_add_u32 s18, s18, 0x1000
	s_addc_u32 s19, s19, 0
	s_waitcnt vmcnt(45)
	v_cvt_pk_bf16_f32 v28, v24, v25
	v_cvt_pk_bf16_f32 v29, v26, v27
	v_fma_f32 v24, v168, v24, v164
	v_fma_f32 v25, v169, v25, v165
	v_fma_f32 v26, v170, v26, v166
	v_fma_f32 v27, v171, v27, v167
	global_store_dwordx2 v4, v[28:29], s[20:21]
	s_add_u32 s20, s20, 0x40000
	s_addc_u32 s21, s21, 0
	global_load_dwordx4 v[164:167], v3, s[14:15] nt
	global_load_dwordx4 v[168:171], v5, s[18:19]
	s_add_u32 s14, s14, 0x80000
	s_addc_u32 s15, s15, 0
	s_add_u32 s18, s18, 0x1000
	s_addc_u32 s19, s19, 0
	s_waitcnt vmcnt(45)
	v_cvt_pk_bf16_f32 v28, v24, v25
	v_cvt_pk_bf16_f32 v29, v26, v27
	v_fma_f32 v24, v36, v24, v32
	v_fma_f32 v25, v37, v25, v33
	v_fma_f32 v26, v38, v26, v34
	v_fma_f32 v27, v39, v27, v35
	global_store_dwordx2 v4, v[28:29], s[20:21]
	s_add_u32 s20, s20, 0x40000
	s_addc_u32 s21, s21, 0
	global_load_dwordx4 v[32:35], v3, s[14:15] nt
	global_load_dwordx4 v[36:39], v5, s[18:19]
	s_add_u32 s14, s14, 0x80000
	s_addc_u32 s15, s15, 0
	s_add_u32 s18, s18, 0x1000
	s_addc_u32 s19, s19, 0
	s_waitcnt vmcnt(45)
	v_cvt_pk_bf16_f32 v28, v24, v25
	v_cvt_pk_bf16_f32 v29, v26, v27
	v_fma_f32 v24, v44, v24, v40
	v_fma_f32 v25, v45, v25, v41
	v_fma_f32 v26, v46, v26, v42
	v_fma_f32 v27, v47, v27, v43
	global_store_dwordx2 v4, v[28:29], s[20:21]
	s_add_u32 s20, s20, 0x40000
	s_addc_u32 s21, s21, 0
	global_load_dwordx4 v[40:43], v3, s[14:15] nt
	global_load_dwordx4 v[44:47], v5, s[18:19]
	s_add_u32 s14, s14, 0x80000
	s_addc_u32 s15, s15, 0
	s_add_u32 s18, s18, 0x1000
	s_addc_u32 s19, s19, 0
	s_waitcnt vmcnt(45)
	v_cvt_pk_bf16_f32 v28, v24, v25
	v_cvt_pk_bf16_f32 v29, v26, v27
	v_fma_f32 v24, v52, v24, v48
	v_fma_f32 v25, v53, v25, v49
	v_fma_f32 v26, v54, v26, v50
	v_fma_f32 v27, v55, v27, v51
	global_store_dwordx2 v4, v[28:29], s[20:21]
	s_add_u32 s20, s20, 0x40000
	s_addc_u32 s21, s21, 0
	global_load_dwordx4 v[48:51], v3, s[14:15] nt
	global_load_dwordx4 v[52:55], v5, s[18:19]
	s_add_u32 s14, s14, 0x80000
	s_addc_u32 s15, s15, 0
	s_add_u32 s18, s18, 0x1000
	s_addc_u32 s19, s19, 0
	s_waitcnt vmcnt(45)
	v_cvt_pk_bf16_f32 v28, v24, v25
	v_cvt_pk_bf16_f32 v29, v26, v27
	v_fma_f32 v24, v60, v24, v56
	v_fma_f32 v25, v61, v25, v57
	v_fma_f32 v26, v62, v26, v58
	v_fma_f32 v27, v63, v27, v59
	global_store_dwordx2 v4, v[28:29], s[20:21]
	s_add_u32 s20, s20, 0x40000
	s_addc_u32 s21, s21, 0
	global_load_dwordx4 v[56:59], v3, s[14:15] nt
	global_load_dwordx4 v[60:63], v5, s[18:19]
	s_add_u32 s14, s14, 0x80000
	s_addc_u32 s15, s15, 0
	s_add_u32 s18, s18, 0x1000
	s_addc_u32 s19, s19, 0
	s_waitcnt vmcnt(45)
; #define H2_LOAD(V, D, C0) do { _Pragma("unroll") for (int u = 0; u < 6; ++u) { V[u] = __builtin_nontemporal_load(kv + (size_t)((C0) + u) * 8 * 16384); D[u] = dc[(size_t)((C0) + u) * 8 * 128]; } } while (0)
; #define H2_STEP(V, D, C0) do { _Pragma("unroll") for (int u = 0; u < 6; ++u) { sb[(size_t)((C0) + u) * 8 * 16384] = f2bf(S); S = fmaf(D[u], S, V[u]); } } while (0)
; __device__ __forceinline__ void ph_hgrn_chain2(const P& p, int gt, int nt) {
;     ...
;     H2_LOAD(a, da, 0);
; #pragma unroll 1
;     for (int c0 = 0; c0 < HG_NCH; c0 += 12) {
;       H2_LOAD(b2, db, c0 + 6); H2_STEP(a, da, c0);
;       if (c0 + 12 < HG_NCH) H2_LOAD(a, da, c0 + 12);
;       H2_STEP(b2, db, c0 + 6);
	v_cvt_pk_bf16_f32 v28, v24, v25
	v_cvt_pk_bf16_f32 v29, v26, v27
	v_fma_f32 v24, v76, v24, v72
	v_fma_f32 v25, v77, v25, v73
	v_fma_f32 v26, v78, v26, v74
	v_fma_f32 v27, v79, v27, v75
	global_store_dwordx2 v4, v[28:29], s[20:21]
	s_add_u32 s20, s20, 0x40000
	s_addc_u32 s21, s21, 0
	global_load_dwordx4 v[72:75], v3, s[14:15] nt
	global_load_dwordx4 v[76:79], v5, s[18:19]
	s_add_u32 s14, s14, 0x80000
	s_addc_u32 s15, s15, 0
	s_add_u32 s18, s18, 0x1000
	s_addc_u32 s19, s19, 0
	s_waitcnt vmcnt(45)
	v_cvt_pk_bf16_f32 v28, v24, v25
	v_cvt_pk_bf16_f32 v29, v26, v27
	v_fma_f32 v24, v84, v24, v80
	v_fma_f32 v25, v85, v25, v81
	v_fma_f32 v26, v86, v26, v82
	v_fma_f32 v27, v87, v27, v83
	global_store_dwordx2 v4, v[28:29], s[20:21]
	s_add_u32 s20, s20, 0x40000
	s_addc_u32 s21, s21, 0
	global_load_dwordx4 v[80:83], v3, s[14:15] nt
	global_load_dwordx4 v[84:87], v5, s[18:19]
	s_add_u32 s14, s14, 0x80000
	s_addc_u32 s15, s15, 0
	s_add_u32 s18, s18, 0x1000
	s_addc_u32 s19, s19, 0
	s_waitcnt vmcnt(45)
	v_cvt_pk_bf16_f32 v28, v24, v25
	v_cvt_pk_bf16_f32 v29, v26, v27
	v_fma_f32 v24, v92, v24, v88
	v_fma_f32 v25, v93, v25, v89
	v_fma_f32 v26, v94, v26, v90
	v_fma_f32 v27, v95, v27, v91
	global_store_dwordx2 v4, v[28:29], s[20:21]
	s_add_u32 s20, s20, 0x40000
	s_addc_u32 s21, s21, 0
	global_load_dwordx4 v[88:91], v3, s[14:15] nt
	global_load_dwordx4 v[92:95], v5, s[18:19]
	s_add_u32 s14, s14, 0x80000
	s_addc_u32 s15, s15, 0
	s_add_u32 s18, s18, 0x1000
	s_addc_u32 s19, s19, 0
	s_waitcnt vmcnt(45)
	v_cvt_pk_bf16_f32 v28, v24, v25
	v_cvt_pk_bf16_f32 v29, v26, v27
	v_fma_f32 v24, v104, v24, v100
	v_fma_f32 v25, v105, v25, v101
	v_fma_f32 v26, v106, v26, v102
	v_fma_f32 v27, v107, v27, v103
	global_store_dwordx2 v4, v[28:29], s[20:21]
	s_add_u32 s20, s20, 0x40000
	s_addc_u32 s21, s21, 0
	global_load_dwordx4 v[100:103], v3, s[14:15] nt
	global_load_dwordx4 v[104:107], v5, s[18:19]
	s_add_u32 s14, s14, 0x80000
	s_addc_u32 s15, s15, 0
	s_add_u32 s18, s18, 0x1000
	s_addc_u32 s19, s19, 0
	s_waitcnt vmcnt(45)
	v_cvt_pk_bf16_f32 v28, v24, v25
	v_cvt_pk_bf16_f32 v29, v26, v27
	v_fma_f32 v24, v112, v24, v108
	v_fma_f32 v25, v113, v25, v109
	v_fma_f32 v26, v114, v26, v110
	v_fma_f32 v27, v115, v27, v111
	global_store_dwordx2 v4, v[28:29], s[20:21]
	s_add_u32 s20, s20, 0x40000
	s_addc_u32 s21, s21, 0
	global_load_dwordx4 v[108:111], v3, s[14:15] nt
	global_load_dwordx4 v[112:115], v5, s[18:19]
	s_add_u32 s14, s14, 0x80000
	s_addc_u32 s15, s15, 0
	s_add_u32 s18, s18, 0x1000
	s_addc_u32 s19, s19, 0
	s_waitcnt vmcnt(45)
	v_cvt_pk_bf16_f32 v28, v24, v25
	v_cvt_pk_bf16_f32 v29, v26, v27
	v_fma_f32 v24, v120, v24, v116
	v_fma_f32 v25, v121, v25, v117
	v_fma_f32 v26, v122, v26, v118
	v_fma_f32 v27, v123, v27, v119
	global_store_dwordx2 v4, v[28:29], s[20:21]
	s_add_u32 s20, s20, 0x40000
	s_addc_u32 s21, s21, 0
	global_load_dwordx4 v[116:119], v3, s[14:15] nt
	global_load_dwordx4 v[120:123], v5, s[18:19]
	s_add_u32 s14, s14, 0x80000
	s_addc_u32 s15, s15, 0
	s_add_u32 s18, s18, 0x1000
	s_addc_u32 s19, s19, 0
	s_waitcnt vmcnt(45)
	v_cvt_pk_bf16_f32 v28, v24, v25
	v_cvt_pk_bf16_f32 v29, v26, v27
	v_fma_f32 v24, v128, v24, v124
	v_fma_f32 v25, v129, v25, v125
	v_fma_f32 v26, v130, v26, v126
	v_fma_f32 v27, v131, v27, v127
	global_store_dwordx2 v4, v[28:29], s[20:21]
	s_add_u32 s20, s20, 0x40000
	s_addc_u32 s21, s21, 0
	global_load_dwordx4 v[124:127], v3, s[14:15] nt
	global_load_dwordx4 v[128:131], v5, s[18:19]
	s_add_u32 s14, s14, 0x80000
	s_addc_u32 s15, s15, 0
	s_add_u32 s18, s18, 0x1000
	s_addc_u32 s19, s19, 0
	s_waitcnt vmcnt(45)
	v_cvt_pk_bf16_f32 v28, v24, v25
	v_cvt_pk_bf16_f32 v29, v26, v27
	v_fma_f32 v24, v136, v24, v132
	v_fma_f32 v25, v137, v25, v133
	v_fma_f32 v26, v138, v26, v134
	v_fma_f32 v27, v139, v27, v135
	global_store_dwordx2 v4, v[28:29], s[20:21]
	s_add_u32 s20, s20, 0x40000
	s_addc_u32 s21, s21, 0
	global_load_dwordx4 v[132:135], v3, s[14:15] nt
	global_load_dwordx4 v[136:139], v5, s[18:19]
	s_add_u32 s14, s14, 0x80000
	s_addc_u32 s15, s15, 0
	s_add_u32 s18, s18, 0x1000
	s_addc_u32 s19, s19, 0
	s_waitcnt vmcnt(45)
	v_cvt_pk_bf16_f32 v28, v24, v25
	v_cvt_pk_bf16_f32 v29, v26, v27
	v_fma_f32 v24, v144, v24, v140
	v_fma_f32 v25, v145, v25, v141
	v_fma_f32 v26, v146, v26, v142
	v_fma_f32 v27, v147, v27, v143
	global_store_dwordx2 v4, v[28:29], s[20:21]
	s_add_u32 s20, s20, 0x40000
	s_addc_u32 s21, s21, 0
	global_load_dwordx4 v[140:143], v3, s[14:15] nt
	global_load_dwordx4 v[144:147], v5, s[18:19]
	s_add_u32 s14, s14, 0x80000
	s_addc_u32 s15, s15, 0
	s_add_u32 s18, s18, 0x1000
	s_addc_u32 s19, s19, 0
	s_waitcnt vmcnt(45)
	v_cvt_pk_bf16_f32 v28, v24, v25
	v_cvt_pk_bf16_f32 v29, v26, v27
	v_fma_f32 v24, v152, v24, v148
	v_fma_f32 v25, v153, v25, v149
	v_fma_f32 v26, v154, v26, v150
	v_fma_f32 v27, v155, v27, v151
	global_store_dwordx2 v4, v[28:29], s[20:21]
	s_add_u32 s20, s20, 0x40000
	s_addc_u32 s21, s21, 0
	global_load_dwordx4 v[148:151], v3, s[14:15] nt
	global_load_dwordx4 v[152:155], v5, s[18:19]
	s_add_u32 s14, s14, 0x80000
	s_addc_u32 s15, s15, 0
	s_add_u32 s18, s18, 0x1000
	s_addc_u32 s19, s19, 0
	s_waitcnt vmcnt(45)
	v_cvt_pk_bf16_f32 v28, v24, v25
	v_cvt_pk_bf16_f32 v29, v26, v27
	v_fma_f32 v24, v160, v24, v156
	v_fma_f32 v25, v161, v25, v157
	v_fma_f32 v26, v162, v26, v158
	v_fma_f32 v27, v163, v27, v159
	global_store_dwordx2 v4, v[28:29], s[20:21]
	s_add_u32 s20, s20, 0x40000
	s_addc_u32 s21, s21, 0
	global_load_dwordx4 v[156:159], v3, s[14:15] nt
	global_load_dwordx4 v[160:163], v5, s[18:19]
	s_add_u32 s14, s14, 0x80000
	s_addc_u32 s15, s15, 0
	s_add_u32 s18, s18, 0x1000
	s_addc_u32 s19, s19, 0
	s_waitcnt vmcnt(45)
; #define H2_LOAD(V, D, C0) do { _Pragma("unroll") for (int u = 0; u < 6; ++u) { V[u] = __builtin_nontemporal_load(kv + (size_t)((C0) + u) * 8 * 16384); D[u] = dc[(size_t)((C0) + u) * 8 * 128]; } } while (0)
; #define H2_STEP(V, D, C0) do { _Pragma("unroll") for (int u = 0; u < 6; ++u) { sb[(size_t)((C0) + u) * 8 * 16384] = f2bf(S); S = fmaf(D[u], S, V[u]); } } while (0)
; __device__ __forceinline__ void ph_hgrn_chain2(const P& p, int gt, int nt) {
;     ...
;     H2_LOAD(a, da, 0);
; #pragma unroll 1
;     for (int c0 = 0; c0 < HG_NCH; c0 += 12) {
;       H2_LOAD(b2, db, c0 + 6); H2_STEP(a, da, c0);
;       if (c0 + 12 < HG_NCH) H2_LOAD(a, da, c0 + 12);
;       H2_STEP(b2, db, c0 + 6);
	v_cvt_pk_bf16_f32 v28, v24, v25
	v_cvt_pk_bf16_f32 v29, v26, v27
	v_fma_f32 v24, v168, v24, v164
	v_fma_f32 v25, v169, v25, v165
	v_fma_f32 v26, v170, v26, v166
	v_fma_f32 v27, v171, v27, v167
	global_store_dwordx2 v4, v[28:29], s[20:21]
	s_add_u32 s20, s20, 0x40000
	s_addc_u32 s21, s21, 0
	global_load_dwordx4 v[164:167], v3, s[14:15] nt
	global_load_dwordx4 v[168:171], v5, s[18:19]
	s_add_u32 s14, s14, 0x80000
	s_addc_u32 s15, s15, 0
	s_add_u32 s18, s18, 0x1000
	s_addc_u32 s19, s19, 0
	s_waitcnt vmcnt(45)
	v_cvt_pk_bf16_f32 v28, v24, v25
	v_cvt_pk_bf16_f32 v29, v26, v27
	v_fma_f32 v24, v36, v24, v32
	v_fma_f32 v25, v37, v25, v33
	v_fma_f32 v26, v38, v26, v34
	v_fma_f32 v27, v39, v27, v35
	global_store_dwordx2 v4, v[28:29], s[20:21]
	s_add_u32 s20, s20, 0x40000
	s_addc_u32 s21, s21, 0
	global_load_dwordx4 v[32:35], v3, s[14:15] nt
	global_load_dwordx4 v[36:39], v5, s[18:19]
	s_add_u32 s14, s14, 0x80000
	s_addc_u32 s15, s15, 0
	s_add_u32 s18, s18, 0x1000
	s_addc_u32 s19, s19, 0
	s_waitcnt vmcnt(45)
	v_cvt_pk_bf16_f32 v28, v24, v25
	v_cvt_pk_bf16_f32 v29, v26, v27
	v_fma_f32 v24, v44, v24, v40
	v_fma_f32 v25, v45, v25, v41
	v_fma_f32 v26, v46, v26, v42
	v_fma_f32 v27, v47, v27, v43
	global_store_dwordx2 v4, v[28:29], s[20:21]
	s_add_u32 s20, s20, 0x40000
	s_addc_u32 s21, s21, 0
	global_load_dwordx4 v[40:43], v3, s[14:15] nt
	global_load_dwordx4 v[44:47], v5, s[18:19]
	s_add_u32 s14, s14, 0x80000
	s_addc_u32 s15, s15, 0
	s_add_u32 s18, s18, 0x1000
	s_addc_u32 s19, s19, 0
	s_waitcnt vmcnt(45)
	v_cvt_pk_bf16_f32 v28, v24, v25
	v_cvt_pk_bf16_f32 v29, v26, v27
	v_fma_f32 v24, v52, v24, v48
	v_fma_f32 v25, v53, v25, v49
	v_fma_f32 v26, v54, v26, v50
	v_fma_f32 v27, v55, v27, v51
	global_store_dwordx2 v4, v[28:29], s[20:21]
	s_add_u32 s20, s20, 0x40000
	s_addc_u32 s21, s21, 0
	global_load_dwordx4 v[48:51], v3, s[14:15] nt
	global_load_dwordx4 v[52:55], v5, s[18:19]
	s_add_u32 s14, s14, 0x80000
	s_addc_u32 s15, s15, 0
	s_add_u32 s18, s18, 0x1000
	s_addc_u32 s19, s19, 0
	s_waitcnt vmcnt(45)
	v_cvt_pk_bf16_f32 v28, v24, v25
	v_cvt_pk_bf16_f32 v29, v26, v27
	v_fma_f32 v24, v60, v24, v56
	v_fma_f32 v25, v61, v25, v57
	v_fma_f32 v26, v62, v26, v58
	v_fma_f32 v27, v63, v27, v59
	global_store_dwordx2 v4, v[28:29], s[20:21]
	s_add_u32 s20, s20, 0x40000
	s_addc_u32 s21, s21, 0
	global_load_dwordx4 v[56:59], v3, s[14:15] nt
	global_load_dwordx4 v[60:63], v5, s[18:19]
	s_add_u32 s14, s14, 0x80000
	s_addc_u32 s15, s15, 0
	s_add_u32 s18, s18, 0x1000
	s_addc_u32 s19, s19, 0
	s_waitcnt vmcnt(45)
	v_cvt_pk_bf16_f32 v28, v24, v25
	v_cvt_pk_bf16_f32 v29, v26, v27
	v_fma_f32 v24, v76, v24, v72
	v_fma_f32 v25, v77, v25, v73
	v_fma_f32 v26, v78, v26, v74
	v_fma_f32 v27, v79, v27, v75
	global_store_dwordx2 v4, v[28:29], s[20:21]
	s_add_u32 s20, s20, 0x40000
	s_addc_u32 s21, s21, 0
	global_load_dwordx4 v[72:75], v3, s[14:15] nt
	global_load_dwordx4 v[76:79], v5, s[18:19]
	s_add_u32 s14, s14, 0x80000
	s_addc_u32 s15, s15, 0
	s_add_u32 s18, s18, 0x1000
	s_addc_u32 s19, s19, 0
	s_waitcnt vmcnt(45)
	v_cvt_pk_bf16_f32 v28, v24, v25
	v_cvt_pk_bf16_f32 v29, v26, v27
	v_fma_f32 v24, v84, v24, v80
	v_fma_f32 v25, v85, v25, v81
	v_fma_f32 v26, v86, v26, v82
	v_fma_f32 v27, v87, v27, v83
	global_store_dwordx2 v4, v[28:29], s[20:21]
	s_add_u32 s20, s20, 0x40000
	s_addc_u32 s21, s21, 0
	global_load_dwordx4 v[80:83], v3, s[14:15] nt
	global_load_dwordx4 v[84:87], v5, s[18:19]
	s_add_u32 s14, s14, 0x80000
	s_addc_u32 s15, s15, 0
	s_add_u32 s18, s18, 0x1000
	s_addc_u32 s19, s19, 0
	s_waitcnt vmcnt(45)
	v_cvt_pk_bf16_f32 v28, v24, v25
	v_cvt_pk_bf16_f32 v29, v26, v27
	v_fma_f32 v24, v92, v24, v88
	v_fma_f32 v25, v93, v25, v89
	v_fma_f32 v26, v94, v26, v90
	v_fma_f32 v27, v95, v27, v91
	global_store_dwordx2 v4, v[28:29], s[20:21]
	s_add_u32 s20, s20, 0x40000
	s_addc_u32 s21, s21, 0
	global_load_dwordx4 v[88:91], v3, s[14:15] nt
	global_load_dwordx4 v[92:95], v5, s[18:19]
	s_add_u32 s14, s14, 0x80000
	s_addc_u32 s15, s15, 0
	s_add_u32 s18, s18, 0x1000
	s_addc_u32 s19, s19, 0
	s_waitcnt vmcnt(45)
	v_cvt_pk_bf16_f32 v28, v24, v25
	v_cvt_pk_bf16_f32 v29, v26, v27
	v_fma_f32 v24, v104, v24, v100
	v_fma_f32 v25, v105, v25, v101
	v_fma_f32 v26, v106, v26, v102
	v_fma_f32 v27, v107, v27, v103
	global_store_dwordx2 v4, v[28:29], s[20:21]
	s_add_u32 s20, s20, 0x40000
	s_addc_u32 s21, s21, 0
	global_load_dwordx4 v[100:103], v3, s[14:15] nt
	global_load_dwordx4 v[104:107], v5, s[18:19]
	s_add_u32 s14, s14, 0x80000
	s_addc_u32 s15, s15, 0
	s_add_u32 s18, s18, 0x1000
	s_addc_u32 s19, s19, 0
	s_waitcnt vmcnt(45)
	v_cvt_pk_bf16_f32 v28, v24, v25
	v_cvt_pk_bf16_f32 v29, v26, v27
	v_fma_f32 v24, v112, v24, v108
	v_fma_f32 v25, v113, v25, v109
	v_fma_f32 v26, v114, v26, v110
	v_fma_f32 v27, v115, v27, v111
	global_store_dwordx2 v4, v[28:29], s[20:21]
	s_add_u32 s20, s20, 0x40000
	s_addc_u32 s21, s21, 0
	global_load_dwordx4 v[108:111], v3, s[14:15] nt
	global_load_dwordx4 v[112:115], v5, s[18:19]
	s_add_u32 s14, s14, 0x80000
	s_addc_u32 s15, s15, 0
	s_add_u32 s18, s18, 0x1000
	s_addc_u32 s19, s19, 0
	s_waitcnt vmcnt(45)
	v_cvt_pk_bf16_f32 v28, v24, v25
	v_cvt_pk_bf16_f32 v29, v26, v27
	v_fma_f32 v24, v120, v24, v116
	v_fma_f32 v25, v121, v25, v117
	v_fma_f32 v26, v122, v26, v118
	v_fma_f32 v27, v123, v27, v119
	global_store_dwordx2 v4, v[28:29], s[20:21]
	s_add_u32 s20, s20, 0x40000
	s_addc_u32 s21, s21, 0
	global_load_dwordx4 v[116:119], v3, s[14:15] nt
	global_load_dwordx4 v[120:123], v5, s[18:19]
	s_add_u32 s14, s14, 0x80000
	s_addc_u32 s15, s15, 0
	s_add_u32 s18, s18, 0x1000
	s_addc_u32 s19, s19, 0
	s_waitcnt vmcnt(45)
; #define H2_LOAD(V, D, C0) do { _Pragma("unroll") for (int u = 0; u < 6; ++u) { V[u] = __builtin_nontemporal_load(kv + (size_t)((C0) + u) * 8 * 16384); D[u] = dc[(size_t)((C0) + u) * 8 * 128]; } } while (0)
; #define H2_STEP(V, D, C0) do { _Pragma("unroll") for (int u = 0; u < 6; ++u) { sb[(size_t)((C0) + u) * 8 * 16384] = f2bf(S); S = fmaf(D[u], S, V[u]); } } while (0)
; __device__ __forceinline__ void ph_hgrn_chain2(const P& p, int gt, int nt) {
;     ...
;     H2_LOAD(a, da, 0);
; #pragma unroll 1
;     for (int c0 = 0; c0 < HG_NCH; c0 += 12) {
;       H2_LOAD(b2, db, c0 + 6); H2_STEP(a, da, c0);
;       if (c0 + 12 < HG_NCH) H2_LOAD(a, da, c0 + 12);
;       H2_STEP(b2, db, c0 + 6);
	v_cvt_pk_bf16_f32 v28, v24, v25
	v_cvt_pk_bf16_f32 v29, v26, v27
	v_fma_f32 v24, v128, v24, v124
	v_fma_f32 v25, v129, v25, v125
	v_fma_f32 v26, v130, v26, v126
	v_fma_f32 v27, v131, v27, v127
	global_store_dwordx2 v4, v[28:29], s[20:21]
	s_add_u32 s20, s20, 0x40000
	s_addc_u32 s21, s21, 0
	global_load_dwordx4 v[124:127], v3, s[14:15] nt
	global_load_dwordx4 v[128:131], v5, s[18:19]
	s_add_u32 s14, s14, 0x80000
	s_addc_u32 s15, s15, 0
	s_add_u32 s18, s18, 0x1000
	s_addc_u32 s19, s19, 0
	s_waitcnt vmcnt(45)
	v_cvt_pk_bf16_f32 v28, v24, v25
	v_cvt_pk_bf16_f32 v29, v26, v27
	v_fma_f32 v24, v136, v24, v132
	v_fma_f32 v25, v137, v25, v133
	v_fma_f32 v26, v138, v26, v134
	v_fma_f32 v27, v139, v27, v135
	global_store_dwordx2 v4, v[28:29], s[20:21]
	s_add_u32 s20, s20, 0x40000
	s_addc_u32 s21, s21, 0
	global_load_dwordx4 v[132:135], v3, s[14:15] nt
	global_load_dwordx4 v[136:139], v5, s[18:19]
	s_add_u32 s14, s14, 0x80000
	s_addc_u32 s15, s15, 0
	s_add_u32 s18, s18, 0x1000
	s_addc_u32 s19, s19, 0
	s_waitcnt vmcnt(45)
	v_cvt_pk_bf16_f32 v28, v24, v25
	v_cvt_pk_bf16_f32 v29, v26, v27
	v_fma_f32 v24, v144, v24, v140
	v_fma_f32 v25, v145, v25, v141
	v_fma_f32 v26, v146, v26, v142
	v_fma_f32 v27, v147, v27, v143
	global_store_dwordx2 v4, v[28:29], s[20:21]
	s_add_u32 s20, s20, 0x40000
	s_addc_u32 s21, s21, 0
	global_load_dwordx4 v[140:143], v3, s[14:15] nt
	global_load_dwordx4 v[144:147], v5, s[18:19]
	s_add_u32 s14, s14, 0x80000
	s_addc_u32 s15, s15, 0
	s_add_u32 s18, s18, 0x1000
	s_addc_u32 s19, s19, 0
	s_waitcnt vmcnt(45)
	v_cvt_pk_bf16_f32 v28, v24, v25
	v_cvt_pk_bf16_f32 v29, v26, v27
	v_fma_f32 v24, v152, v24, v148
	v_fma_f32 v25, v153, v25, v149
	v_fma_f32 v26, v154, v26, v150
	v_fma_f32 v27, v155, v27, v151
	global_store_dwordx2 v4, v[28:29], s[20:21]
	s_add_u32 s20, s20, 0x40000
	s_addc_u32 s21, s21, 0
	global_load_dwordx4 v[148:151], v3, s[14:15] nt
	global_load_dwordx4 v[152:155], v5, s[18:19]
	s_add_u32 s14, s14, 0x80000
	s_addc_u32 s15, s15, 0
	s_add_u32 s18, s18, 0x1000
	s_addc_u32 s19, s19, 0
	s_waitcnt vmcnt(45)
	v_cvt_pk_bf16_f32 v28, v24, v25
	v_cvt_pk_bf16_f32 v29, v26, v27
	v_fma_f32 v24, v160, v24, v156
	v_fma_f32 v25, v161, v25, v157
	v_fma_f32 v26, v162, v26, v158
	v_fma_f32 v27, v163, v27, v159
	global_store_dwordx2 v4, v[28:29], s[20:21]
	s_add_u32 s20, s20, 0x40000
	s_addc_u32 s21, s21, 0
	global_load_dwordx4 v[156:159], v3, s[14:15] nt
	global_load_dwordx4 v[160:163], v5, s[18:19]
	s_add_u32 s14, s14, 0x80000
	s_addc_u32 s15, s15, 0
	s_add_u32 s18, s18, 0x1000
	s_addc_u32 s19, s19, 0
	s_waitcnt vmcnt(45)
	v_cvt_pk_bf16_f32 v28, v24, v25
	v_cvt_pk_bf16_f32 v29, v26, v27
	v_fma_f32 v24, v168, v24, v164
	v_fma_f32 v25, v169, v25, v165
	v_fma_f32 v26, v170, v26, v166
	v_fma_f32 v27, v171, v27, v167
	global_store_dwordx2 v4, v[28:29], s[20:21]
	s_add_u32 s20, s20, 0x40000
	s_addc_u32 s21, s21, 0
	global_load_dwordx4 v[164:167], v3, s[14:15] nt
	global_load_dwordx4 v[168:171], v5, s[18:19]
	s_add_u32 s14, s14, 0x80000
	s_addc_u32 s15, s15, 0
	s_add_u32 s18, s18, 0x1000
	s_addc_u32 s19, s19, 0
	s_waitcnt vmcnt(45)
	v_cvt_pk_bf16_f32 v28, v24, v25
	v_cvt_pk_bf16_f32 v29, v26, v27
	v_fma_f32 v24, v36, v24, v32
	v_fma_f32 v25, v37, v25, v33
	v_fma_f32 v26, v38, v26, v34
	v_fma_f32 v27, v39, v27, v35
	global_store_dwordx2 v4, v[28:29], s[20:21]
	s_add_u32 s20, s20, 0x40000
	s_addc_u32 s21, s21, 0
	global_load_dwordx4 v[32:35], v3, s[14:15] nt
	global_load_dwordx4 v[36:39], v5, s[18:19]
	s_add_u32 s14, s14, 0x80000
	s_addc_u32 s15, s15, 0
	s_add_u32 s18, s18, 0x1000
	s_addc_u32 s19, s19, 0
	s_waitcnt vmcnt(45)
	v_cvt_pk_bf16_f32 v28, v24, v25
	v_cvt_pk_bf16_f32 v29, v26, v27
	v_fma_f32 v24, v44, v24, v40
	v_fma_f32 v25, v45, v25, v41
	v_fma_f32 v26, v46, v26, v42
	v_fma_f32 v27, v47, v27, v43
	global_store_dwordx2 v4, v[28:29], s[20:21]
	s_add_u32 s20, s20, 0x40000
	s_addc_u32 s21, s21, 0
	global_load_dwordx4 v[40:43], v3, s[14:15] nt
	global_load_dwordx4 v[44:47], v5, s[18:19]
	s_add_u32 s14, s14, 0x80000
	s_addc_u32 s15, s15, 0
	s_add_u32 s18, s18, 0x1000
	s_addc_u32 s19, s19, 0
	s_waitcnt vmcnt(45)
	v_cvt_pk_bf16_f32 v28, v24, v25
	v_cvt_pk_bf16_f32 v29, v26, v27
	v_fma_f32 v24, v52, v24, v48
	v_fma_f32 v25, v53, v25, v49
	v_fma_f32 v26, v54, v26, v50
	v_fma_f32 v27, v55, v27, v51
	global_store_dwordx2 v4, v[28:29], s[20:21]
	s_add_u32 s20, s20, 0x40000
	s_addc_u32 s21, s21, 0
	global_load_dwordx4 v[48:51], v3, s[14:15] nt
	global_load_dwordx4 v[52:55], v5, s[18:19]
	s_add_u32 s14, s14, 0x80000
	s_addc_u32 s15, s15, 0
	s_add_u32 s18, s18, 0x1000
	s_addc_u32 s19, s19, 0
	s_waitcnt vmcnt(45)
	v_cvt_pk_bf16_f32 v28, v24, v25
	v_cvt_pk_bf16_f32 v29, v26, v27
	v_fma_f32 v24, v60, v24, v56
	v_fma_f32 v25, v61, v25, v57
	v_fma_f32 v26, v62, v26, v58
	v_fma_f32 v27, v63, v27, v59
	global_store_dwordx2 v4, v[28:29], s[20:21]
	s_add_u32 s20, s20, 0x40000
	s_addc_u32 s21, s21, 0
	global_load_dwordx4 v[56:59], v3, s[14:15] nt
	global_load_dwordx4 v[60:63], v5, s[18:19]
	s_add_u32 s14, s14, 0x80000
	s_addc_u32 s15, s15, 0
	s_add_u32 s18, s18, 0x1000
	s_addc_u32 s19, s19, 0
	s_waitcnt vmcnt(45)
	v_cvt_pk_bf16_f32 v28, v24, v25
	v_cvt_pk_bf16_f32 v29, v26, v27
	v_fma_f32 v24, v76, v24, v72
	v_fma_f32 v25, v77, v25, v73
	v_fma_f32 v26, v78, v26, v74
	v_fma_f32 v27, v79, v27, v75
	global_store_dwordx2 v4, v[28:29], s[20:21]
	s_add_u32 s20, s20, 0x40000
	s_addc_u32 s21, s21, 0
	global_load_dwordx4 v[72:75], v3, s[14:15] nt
	global_load_dwordx4 v[76:79], v5, s[18:19]
	s_add_u32 s14, s14, 0x80000
	s_addc_u32 s15, s15, 0
	s_add_u32 s18, s18, 0x1000
	s_addc_u32 s19, s19, 0
	s_waitcnt vmcnt(45)
; #define H2_LOAD(V, D, C0) do { _Pragma("unroll") for (int u = 0; u < 6; ++u) { V[u] = __builtin_nontemporal_load(kv + (size_t)((C0) + u) * 8 * 16384); D[u] = dc[(size_t)((C0) + u) * 8 * 128]; } } while (0)
; #define H2_STEP(V, D, C0) do { _Pragma("unroll") for (int u = 0; u < 6; ++u) { sb[(size_t)((C0) + u) * 8 * 16384] = f2bf(S); S = fmaf(D[u], S, V[u]); } } while (0)
; __device__ __forceinline__ void ph_hgrn_chain2(const P& p, int gt, int nt) {
;     ...
;     H2_LOAD(a, da, 0);
; #pragma unroll 1
;     for (int c0 = 0; c0 < HG_NCH; c0 += 12) {
;       H2_LOAD(b2, db, c0 + 6); H2_STEP(a, da, c0);
;       if (c0 + 12 < HG_NCH) H2_LOAD(a, da, c0 + 12);
;       H2_STEP(b2, db, c0 + 6);
	v_cvt_pk_bf16_f32 v28, v24, v25
	v_cvt_pk_bf16_f32 v29, v26, v27
	v_fma_f32 v24, v84, v24, v80
	v_fma_f32 v25, v85, v25, v81
	v_fma_f32 v26, v86, v26, v82
	v_fma_f32 v27, v87, v27, v83
	global_store_dwordx2 v4, v[28:29], s[20:21]
	s_add_u32 s20, s20, 0x40000
	s_addc_u32 s21, s21, 0
	global_load_dwordx4 v[80:83], v3, s[14:15] nt
	global_load_dwordx4 v[84:87], v5, s[18:19]
	s_add_u32 s14, s14, 0x80000
	s_addc_u32 s15, s15, 0
	s_add_u32 s18, s18, 0x1000
	s_addc_u32 s19, s19, 0
	s_waitcnt vmcnt(45)
	v_cvt_pk_bf16_f32 v28, v24, v25
	v_cvt_pk_bf16_f32 v29, v26, v27
	v_fma_f32 v24, v92, v24, v88
	v_fma_f32 v25, v93, v25, v89
	v_fma_f32 v26, v94, v26, v90
	v_fma_f32 v27, v95, v27, v91
	global_store_dwordx2 v4, v[28:29], s[20:21]
	s_add_u32 s20, s20, 0x40000
	s_addc_u32 s21, s21, 0
	global_load_dwordx4 v[88:91], v3, s[14:15] nt
	global_load_dwordx4 v[92:95], v5, s[18:19]
	s_add_u32 s14, s14, 0x80000
	s_addc_u32 s15, s15, 0
	s_add_u32 s18, s18, 0x1000
	s_addc_u32 s19, s19, 0
	s_waitcnt vmcnt(45)
	v_cvt_pk_bf16_f32 v28, v24, v25
	v_cvt_pk_bf16_f32 v29, v26, v27
	v_fma_f32 v24, v104, v24, v100
	v_fma_f32 v25, v105, v25, v101
	v_fma_f32 v26, v106, v26, v102
	v_fma_f32 v27, v107, v27, v103
	global_store_dwordx2 v4, v[28:29], s[20:21]
	s_add_u32 s20, s20, 0x40000
	s_addc_u32 s21, s21, 0
	global_load_dwordx4 v[100:103], v3, s[14:15] nt
	global_load_dwordx4 v[104:107], v5, s[18:19]
	s_add_u32 s14, s14, 0x80000
	s_addc_u32 s15, s15, 0
	s_add_u32 s18, s18, 0x1000
	s_addc_u32 s19, s19, 0
	s_waitcnt vmcnt(45)
	v_cvt_pk_bf16_f32 v28, v24, v25
	v_cvt_pk_bf16_f32 v29, v26, v27
	v_fma_f32 v24, v112, v24, v108
	v_fma_f32 v25, v113, v25, v109
	v_fma_f32 v26, v114, v26, v110
	v_fma_f32 v27, v115, v27, v111
	global_store_dwordx2 v4, v[28:29], s[20:21]
	s_add_u32 s20, s20, 0x40000
	s_addc_u32 s21, s21, 0
	global_load_dwordx4 v[108:111], v3, s[14:15] nt
	global_load_dwordx4 v[112:115], v5, s[18:19]
	s_add_u32 s14, s14, 0x80000
	s_addc_u32 s15, s15, 0
	s_add_u32 s18, s18, 0x1000
	s_addc_u32 s19, s19, 0
	s_waitcnt vmcnt(45)
	v_cvt_pk_bf16_f32 v28, v24, v25
	v_cvt_pk_bf16_f32 v29, v26, v27
	v_fma_f32 v24, v120, v24, v116
	v_fma_f32 v25, v121, v25, v117
	v_fma_f32 v26, v122, v26, v118
	v_fma_f32 v27, v123, v27, v119
	global_store_dwordx2 v4, v[28:29], s[20:21]
	s_add_u32 s20, s20, 0x40000
	s_addc_u32 s21, s21, 0
	global_load_dwordx4 v[116:119], v3, s[14:15] nt
	global_load_dwordx4 v[120:123], v5, s[18:19]
	s_add_u32 s14, s14, 0x80000
	s_addc_u32 s15, s15, 0
	s_add_u32 s18, s18, 0x1000
	s_addc_u32 s19, s19, 0
	s_waitcnt vmcnt(45)
	v_cvt_pk_bf16_f32 v28, v24, v25
	v_cvt_pk_bf16_f32 v29, v26, v27
	v_fma_f32 v24, v128, v24, v124
	v_fma_f32 v25, v129, v25, v125
	v_fma_f32 v26, v130, v26, v126
	v_fma_f32 v27, v131, v27, v127
	global_store_dwordx2 v4, v[28:29], s[20:21]
	s_add_u32 s20, s20, 0x40000
	s_addc_u32 s21, s21, 0
	global_load_dwordx4 v[124:127], v3, s[14:15] nt
	global_load_dwordx4 v[128:131], v5, s[18:19]
	s_add_u32 s14, s14, 0x80000
	s_addc_u32 s15, s15, 0
	s_add_u32 s18, s18, 0x1000
	s_addc_u32 s19, s19, 0
	s_waitcnt vmcnt(45)
	v_cvt_pk_bf16_f32 v28, v24, v25
	v_cvt_pk_bf16_f32 v29, v26, v27
	v_fma_f32 v24, v136, v24, v132
	v_fma_f32 v25, v137, v25, v133
	v_fma_f32 v26, v138, v26, v134
	v_fma_f32 v27, v139, v27, v135
	global_store_dwordx2 v4, v[28:29], s[20:21]
	s_add_u32 s20, s20, 0x40000
	s_addc_u32 s21, s21, 0
	global_load_dwordx4 v[132:135], v3, s[14:15] nt
	global_load_dwordx4 v[136:139], v5, s[18:19]
	s_add_u32 s14, s14, 0x80000
	s_addc_u32 s15, s15, 0
	s_add_u32 s18, s18, 0x1000
	s_addc_u32 s19, s19, 0
	s_waitcnt vmcnt(45)
	v_cvt_pk_bf16_f32 v28, v24, v25
	v_cvt_pk_bf16_f32 v29, v26, v27
	v_fma_f32 v24, v144, v24, v140
	v_fma_f32 v25, v145, v25, v141
	v_fma_f32 v26, v146, v26, v142
	v_fma_f32 v27, v147, v27, v143
	global_store_dwordx2 v4, v[28:29], s[20:21]
	s_add_u32 s20, s20, 0x40000
	s_addc_u32 s21, s21, 0
	global_load_dwordx4 v[140:143], v3, s[14:15] nt
	global_load_dwordx4 v[144:147], v5, s[18:19]
	s_add_u32 s14, s14, 0x80000
	s_addc_u32 s15, s15, 0
	s_add_u32 s18, s18, 0x1000
	s_addc_u32 s19, s19, 0
	s_waitcnt vmcnt(45)
	v_cvt_pk_bf16_f32 v28, v24, v25
	v_cvt_pk_bf16_f32 v29, v26, v27
	v_fma_f32 v24, v152, v24, v148
	v_fma_f32 v25, v153, v25, v149
	v_fma_f32 v26, v154, v26, v150
	v_fma_f32 v27, v155, v27, v151
	global_store_dwordx2 v4, v[28:29], s[20:21]
	s_add_u32 s20, s20, 0x40000
	s_addc_u32 s21, s21, 0
	global_load_dwordx4 v[148:151], v3, s[14:15] nt
	global_load_dwordx4 v[152:155], v5, s[18:19]
	s_add_u32 s14, s14, 0x80000
	s_addc_u32 s15, s15, 0
	s_add_u32 s18, s18, 0x1000
	s_addc_u32 s19, s19, 0
	s_waitcnt vmcnt(45)
	v_cvt_pk_bf16_f32 v28, v24, v25
	v_cvt_pk_bf16_f32 v29, v26, v27
	v_fma_f32 v24, v160, v24, v156
	v_fma_f32 v25, v161, v25, v157
	v_fma_f32 v26, v162, v26, v158
	v_fma_f32 v27, v163, v27, v159
	global_store_dwordx2 v4, v[28:29], s[20:21]
	s_add_u32 s20, s20, 0x40000
	s_addc_u32 s21, s21, 0
	global_load_dwordx4 v[156:159], v3, s[14:15] nt
	global_load_dwordx4 v[160:163], v5, s[18:19]
	s_add_u32 s14, s14, 0x80000
	s_addc_u32 s15, s15, 0
	s_add_u32 s18, s18, 0x1000
	s_addc_u32 s19, s19, 0
	s_waitcnt vmcnt(45)
	v_cvt_pk_bf16_f32 v28, v24, v25
	v_cvt_pk_bf16_f32 v29, v26, v27
	v_fma_f32 v24, v168, v24, v164
	v_fma_f32 v25, v169, v25, v165
	v_fma_f32 v26, v170, v26, v166
	v_fma_f32 v27, v171, v27, v167
	global_store_dwordx2 v4, v[28:29], s[20:21]
	s_add_u32 s20, s20, 0x40000
	s_addc_u32 s21, s21, 0
	global_load_dwordx4 v[164:167], v3, s[14:15] nt
	global_load_dwordx4 v[168:171], v5, s[18:19]
	s_add_u32 s14, s14, 0x80000
	s_addc_u32 s15, s15, 0
	s_add_u32 s18, s18, 0x1000
	s_addc_u32 s19, s19, 0
	s_waitcnt vmcnt(45)
; #define H2_LOAD(V, D, C0) do { _Pragma("unroll") for (int u = 0; u < 6; ++u) { V[u] = __builtin_nontemporal_load(kv + (size_t)((C0) + u) * 8 * 16384); D[u] = dc[(size_t)((C0) + u) * 8 * 128]; } } while (0)
; #define H2_STEP(V, D, C0) do { _Pragma("unroll") for (int u = 0; u < 6; ++u) { sb[(size_t)((C0) + u) * 8 * 16384] = f2bf(S); S = fmaf(D[u], S, V[u]); } } while (0)
; __device__ __forceinline__ void ph_hgrn_chain2(const P& p, int gt, int nt) {
;     ...
;     H2_LOAD(a, da, 0);
; #pragma unroll 1
;     for (int c0 = 0; c0 < HG_NCH; c0 += 12) {
;       H2_LOAD(b2, db, c0 + 6); H2_STEP(a, da, c0);
;       if (c0 + 12 < HG_NCH) H2_LOAD(a, da, c0 + 12);
;       H2_STEP(b2, db, c0 + 6);
	v_cvt_pk_bf16_f32 v28, v24, v25
	v_cvt_pk_bf16_f32 v29, v26, v27
	v_fma_f32 v24, v36, v24, v32
	v_fma_f32 v25, v37, v25, v33
	v_fma_f32 v26, v38, v26, v34
	v_fma_f32 v27, v39, v27, v35
	global_store_dwordx2 v4, v[28:29], s[20:21]
	s_add_u32 s20, s20, 0x40000
	s_addc_u32 s21, s21, 0
	global_load_dwordx4 v[32:35], v3, s[14:15] nt
	global_load_dwordx4 v[36:39], v5, s[18:19]
	s_add_u32 s14, s14, 0x80000
	s_addc_u32 s15, s15, 0
	s_add_u32 s18, s18, 0x1000
	s_addc_u32 s19, s19, 0
	s_waitcnt vmcnt(45)
	v_cvt_pk_bf16_f32 v28, v24, v25
	v_cvt_pk_bf16_f32 v29, v26, v27
	v_fma_f32 v24, v44, v24, v40
	v_fma_f32 v25, v45, v25, v41
	v_fma_f32 v26, v46, v26, v42
	v_fma_f32 v27, v47, v27, v43
	global_store_dwordx2 v4, v[28:29], s[20:21]
	s_add_u32 s20, s20, 0x40000
	s_addc_u32 s21, s21, 0
	global_load_dwordx4 v[40:43], v3, s[14:15] nt
	global_load_dwordx4 v[44:47], v5, s[18:19]
	s_add_u32 s14, s14, 0x80000
	s_addc_u32 s15, s15, 0
	s_add_u32 s18, s18, 0x1000
	s_addc_u32 s19, s19, 0
	s_waitcnt vmcnt(45)
	v_cvt_pk_bf16_f32 v28, v24, v25
	v_cvt_pk_bf16_f32 v29, v26, v27
	v_fma_f32 v24, v52, v24, v48
	v_fma_f32 v25, v53, v25, v49
	v_fma_f32 v26, v54, v26, v50
	v_fma_f32 v27, v55, v27, v51
	global_store_dwordx2 v4, v[28:29], s[20:21]
	s_add_u32 s20, s20, 0x40000
	s_addc_u32 s21, s21, 0
	global_load_dwordx4 v[48:51], v3, s[14:15] nt
	global_load_dwordx4 v[52:55], v5, s[18:19]
	s_add_u32 s14, s14, 0x80000
	s_addc_u32 s15, s15, 0
	s_add_u32 s18, s18, 0x1000
	s_addc_u32 s19, s19, 0
	s_waitcnt vmcnt(45)
	v_cvt_pk_bf16_f32 v28, v24, v25
	v_cvt_pk_bf16_f32 v29, v26, v27
	v_fma_f32 v24, v60, v24, v56
	v_fma_f32 v25, v61, v25, v57
	v_fma_f32 v26, v62, v26, v58
	v_fma_f32 v27, v63, v27, v59
	global_store_dwordx2 v4, v[28:29], s[20:21]
	s_add_u32 s20, s20, 0x40000
	s_addc_u32 s21, s21, 0
	global_load_dwordx4 v[56:59], v3, s[14:15] nt
	global_load_dwordx4 v[60:63], v5, s[18:19]
	s_add_u32 s14, s14, 0x80000
	s_addc_u32 s15, s15, 0
	s_add_u32 s18, s18, 0x1000
	s_addc_u32 s19, s19, 0
	s_waitcnt vmcnt(45)
	v_cvt_pk_bf16_f32 v28, v24, v25
	v_cvt_pk_bf16_f32 v29, v26, v27
	v_fma_f32 v24, v76, v24, v72
	v_fma_f32 v25, v77, v25, v73
	v_fma_f32 v26, v78, v26, v74
	v_fma_f32 v27, v79, v27, v75
	global_store_dwordx2 v4, v[28:29], s[20:21]
	s_add_u32 s20, s20, 0x40000
	s_addc_u32 s21, s21, 0
	s_waitcnt vmcnt(43)
	v_cvt_pk_bf16_f32 v28, v24, v25
	v_cvt_pk_bf16_f32 v29, v26, v27
	v_fma_f32 v24, v84, v24, v80
	v_fma_f32 v25, v85, v25, v81
	v_fma_f32 v26, v86, v26, v82
	v_fma_f32 v27, v87, v27, v83
	global_store_dwordx2 v4, v[28:29], s[20:21]
	s_add_u32 s20, s20, 0x40000
	s_addc_u32 s21, s21, 0
	s_waitcnt vmcnt(41)
	v_cvt_pk_bf16_f32 v28, v24, v25
	v_cvt_pk_bf16_f32 v29, v26, v27
	v_fma_f32 v24, v92, v24, v88
	v_fma_f32 v25, v93, v25, v89
	v_fma_f32 v26, v94, v26, v90
	v_fma_f32 v27, v95, v27, v91
	global_store_dwordx2 v4, v[28:29], s[20:21]
	s_add_u32 s20, s20, 0x40000
	s_addc_u32 s21, s21, 0
	s_waitcnt vmcnt(39)
	v_cvt_pk_bf16_f32 v28, v24, v25
	v_cvt_pk_bf16_f32 v29, v26, v27
	v_fma_f32 v24, v104, v24, v100
	v_fma_f32 v25, v105, v25, v101
	v_fma_f32 v26, v106, v26, v102
	v_fma_f32 v27, v107, v27, v103
	global_store_dwordx2 v4, v[28:29], s[20:21]
	s_add_u32 s20, s20, 0x40000
	s_addc_u32 s21, s21, 0
	s_waitcnt vmcnt(37)
	v_cvt_pk_bf16_f32 v28, v24, v25
	v_cvt_pk_bf16_f32 v29, v26, v27
	v_fma_f32 v24, v112, v24, v108
	v_fma_f32 v25, v113, v25, v109
	v_fma_f32 v26, v114, v26, v110
	v_fma_f32 v27, v115, v27, v111
	global_store_dwordx2 v4, v[28:29], s[20:21]
	s_add_u32 s20, s20, 0x40000
	s_addc_u32 s21, s21, 0
	s_waitcnt vmcnt(35)
	v_cvt_pk_bf16_f32 v28, v24, v25
	v_cvt_pk_bf16_f32 v29, v26, v27
	v_fma_f32 v24, v120, v24, v116
	v_fma_f32 v25, v121, v25, v117
	v_fma_f32 v26, v122, v26, v118
	v_fma_f32 v27, v123, v27, v119
	global_store_dwordx2 v4, v[28:29], s[20:21]
	s_add_u32 s20, s20, 0x40000
	s_addc_u32 s21, s21, 0
	s_waitcnt vmcnt(33)
	v_cvt_pk_bf16_f32 v28, v24, v25
	v_cvt_pk_bf16_f32 v29, v26, v27
	v_fma_f32 v24, v128, v24, v124
	v_fma_f32 v25, v129, v25, v125
	v_fma_f32 v26, v130, v26, v126
	v_fma_f32 v27, v131, v27, v127
	global_store_dwordx2 v4, v[28:29], s[20:21]
	s_add_u32 s20, s20, 0x40000
	s_addc_u32 s21, s21, 0
	s_waitcnt vmcnt(31)
	v_cvt_pk_bf16_f32 v28, v24, v25
	v_cvt_pk_bf16_f32 v29, v26, v27
	v_fma_f32 v24, v136, v24, v132
	v_fma_f32 v25, v137, v25, v133
	v_fma_f32 v26, v138, v26, v134
	v_fma_f32 v27, v139, v27, v135
	global_store_dwordx2 v4, v[28:29], s[20:21]
	s_add_u32 s20, s20, 0x40000
	s_addc_u32 s21, s21, 0
	s_waitcnt vmcnt(29)
	v_cvt_pk_bf16_f32 v28, v24, v25
	v_cvt_pk_bf16_f32 v29, v26, v27
	v_fma_f32 v24, v144, v24, v140
	v_fma_f32 v25, v145, v25, v141
	v_fma_f32 v26, v146, v26, v142
	v_fma_f32 v27, v147, v27, v143
	global_store_dwordx2 v4, v[28:29], s[20:21]
	s_add_u32 s20, s20, 0x40000
	s_addc_u32 s21, s21, 0
	s_waitcnt vmcnt(27)
	v_cvt_pk_bf16_f32 v28, v24, v25
	v_cvt_pk_bf16_f32 v29, v26, v27
	v_fma_f32 v24, v152, v24, v148
	v_fma_f32 v25, v153, v25, v149
	v_fma_f32 v26, v154, v26, v150
	v_fma_f32 v27, v155, v27, v151
	global_store_dwordx2 v4, v[28:29], s[20:21]
	s_add_u32 s20, s20, 0x40000
	s_addc_u32 s21, s21, 0
	s_waitcnt vmcnt(25)
	v_cvt_pk_bf16_f32 v28, v24, v25
	v_cvt_pk_bf16_f32 v29, v26, v27
	v_fma_f32 v24, v160, v24, v156
	v_fma_f32 v25, v161, v25, v157
	v_fma_f32 v26, v162, v26, v158
	v_fma_f32 v27, v163, v27, v159
	global_store_dwordx2 v4, v[28:29], s[20:21]
	s_add_u32 s20, s20, 0x40000
	s_addc_u32 s21, s21, 0
	s_waitcnt vmcnt(23)
	v_cvt_pk_bf16_f32 v28, v24, v25
	v_cvt_pk_bf16_f32 v29, v26, v27
	v_fma_f32 v24, v168, v24, v164
	v_fma_f32 v25, v169, v25, v165
	v_fma_f32 v26, v170, v26, v166
	v_fma_f32 v27, v171, v27, v167
	global_store_dwordx2 v4, v[28:29], s[20:21]
	s_add_u32 s20, s20, 0x40000
	s_addc_u32 s21, s21, 0
	s_waitcnt vmcnt(21)
	v_cvt_pk_bf16_f32 v28, v24, v25
	v_cvt_pk_bf16_f32 v29, v26, v27
	v_fma_f32 v24, v36, v24, v32
	v_fma_f32 v25, v37, v25, v33
	v_fma_f32 v26, v38, v26, v34
	v_fma_f32 v27, v39, v27, v35
	global_store_dwordx2 v4, v[28:29], s[20:21]
	s_add_u32 s20, s20, 0x40000
	s_addc_u32 s21, s21, 0
	s_waitcnt vmcnt(19)
	v_cvt_pk_bf16_f32 v28, v24, v25
	v_cvt_pk_bf16_f32 v29, v26, v27
	v_fma_f32 v24, v44, v24, v40
	v_fma_f32 v25, v45, v25, v41
	v_fma_f32 v26, v46, v26, v42
	v_fma_f32 v27, v47, v27, v43
	global_store_dwordx2 v4, v[28:29], s[20:21]
	s_add_u32 s20, s20, 0x40000
	s_addc_u32 s21, s21, 0
	s_waitcnt vmcnt(17)
	v_cvt_pk_bf16_f32 v28, v24, v25
	v_cvt_pk_bf16_f32 v29, v26, v27
	v_fma_f32 v24, v52, v24, v48
	v_fma_f32 v25, v53, v25, v49
	v_fma_f32 v26, v54, v26, v50
	v_fma_f32 v27, v55, v27, v51
	global_store_dwordx2 v4, v[28:29], s[20:21]
	s_add_u32 s20, s20, 0x40000
	s_addc_u32 s21, s21, 0
	s_waitcnt vmcnt(15)
	v_cvt_pk_bf16_f32 v28, v24, v25
	v_cvt_pk_bf16_f32 v29, v26, v27
	v_fma_f32 v24, v60, v24, v56
	v_fma_f32 v25, v61, v25, v57
	v_fma_f32 v26, v62, v26, v58
	v_fma_f32 v27, v63, v27, v59
	global_store_dwordx2 v4, v[28:29], s[20:21]
	s_add_u32 s20, s20, 0x40000
	s_addc_u32 s21, s21, 0
; #define LAS __attribute__((address_space(3)))
; template <bool HALF> __device__ __forceinline__ void unit(const P& p, int l, int u, LAS char* lds, int tid) {
;   int hq, qrow, nk;
;   if (u < 512) { hq = ((u >> 8) << 3) + (u & 7); qrow = CTXL + ((u >> 3) & 31) * 256; nk = NTOK; } else { hq = u - 512; qrow = 0; nk = CTXL; }
;   const int kvh = hq < 8 ? (hq >> 2) : 2 + ((hq - 8) >> 1);
;   const bf16_t* Qb = WSP(bf16_t, WS_PROJ) + (size_t)qrow * INW + (hq < 8 ? C_AQ + hq * 128 : C_DQ + (hq - 8) * 64);
;   const bf16_t* Kh = WSP(bf16_t, WS_KALL) + kvh * 128;
;   const bf16_t* Vh = WSP(bf16_t, WS_PROJ) + (kvh < 2 ? C_AV + kvh * 128 : C_DV + (kvh - 2) * 128);
;   bf16_t* Obf = !HALF ? WSP(bf16_t, WS_MIX) + (size_t)qrow * DM + 512 + hq * 128 : nullptr;
;   float* Of = !HALF ? nullptr : WSP(float, WS_DTMP) + (size_t)qrow * 1024 + (hq - 8) * 128;
; __device__ __forceinline__ void phase(const P& p, int l, bool with_ctx, int G, int bid, LAS char* lds, int tid) {
;   for (int i = bid; i < 256 + (with_ctx ? 8 : 0); i += G) unit<false>(p, l, i < 256 ? i : 512 + (i - 256), lds, tid);
;   for (int i = bid; i < 256 + (with_ctx ? 8 : 0); i += G) unit<true>(p, l, i < 256 ? 256 + i : 520 + (i - 256), lds, tid);
; }
.Lchain_done:
.LBB0_413:
	v_readlane_b32 s2, v255, 18
	v_readlane_b32 s3, v255, 19
	s_and_b64 s[2:3], s[2:3], exec
	s_movk_i32 s2, 0x108
	s_cselect_b32 s5, s2, 0x100
	s_cmp_ge_i32 s88, s5
	s_cbranch_scc1 .LBB0_472
	s_waitcnt lgkmcnt(0)
	s_add_u32 s30, s0, 0x226b4000
	s_addc_u32 s31, s1, 0
	s_add_u32 s44, s0, 0x2cbb4000
	s_addc_u32 s45, s1, 0
	s_lshl_b32 s2, s78, 7
	s_ashr_i32 s3, s2, 31
	s_lshl_b64 s[2:3], s[2:3], 2
	s_add_u32 s14, s12, s2
	s_addc_u32 s15, s13, s3
	s_add_u32 s12, s0, 0x37de2000
	s_addc_u32 s13, s1, 0
	s_mov_b32 s47, s88
	s_branch .LBB0_416
